# speedup vs baseline: 1.0180x; 1.0180x over previous
.Lk4_st4_7:
	v_add_u32_e32 v169, s17, v118
	s_nop 1
	v_readfirstlane_b32 s14, v169
	s_mov_b32 m0, s14
	s_nop 0
	global_load_lds_dwordx4 v[102:103], off nt
	v_add_u32_e32 v169, s17, v90
	s_nop 1
	v_readfirstlane_b32 s14, v169
	s_mov_b32 m0, s14
	s_nop 0
	global_load_lds_dwordx4 v[104:105], off nt
	v_add_u32_e32 v169, s17, v91
	s_nop 1
	v_readfirstlane_b32 s14, v169
	s_mov_b32 m0, s14
	s_nop 0
	global_load_lds_dwordx4 v[108:109], off nt
	v_add_u32_e32 v169, s17, v119
	s_nop 1
	v_readfirstlane_b32 s14, v169
	s_mov_b32 m0, s14
	s_nop 0
	global_load_lds_dwordx4 v[112:113], off nt
	s_add_u32 s52, s10, 0x800000
	s_addc_u32 s53, s11, 0
	v_lshlrev_b32_e32 v169, 2, v98
	v_lshlrev_b32_e32 v170, 2, v100
	global_load_dwordx4 v[128:131], v169, s[52:53] nt
	global_load_dwordx4 v[132:135], v170, s[52:53] nt
	s_add_u32 s52, s10, 0xc00000
	s_addc_u32 s53, s11, 0
	v_lshlrev_b32_e32 v169, 2, v94
	v_lshlrev_b32_e32 v170, 2, v96
	global_load_dwordx4 v[172:175], v169, s[52:53] nt
	global_load_dwordx4 v[176:179], v170, s[52:53] nt
	v_mfma_f32_16x16x32_f16 a[0:3], v[70:73], v[82:85], a[0:3]
	ds_read_b128 v[14:17], v152
	v_mfma_f32_16x16x32_f16 a[4:7], v[70:73], v[86:89], a[4:7]
	ds_read_b128 v[18:21], v154
	v_mfma_f32_16x16x32_f16 a[12:15], v[66:69], v[82:85], a[12:15]
	ds_read_b128 v[42:45], v164
	v_mfma_f32_16x16x32_f16 a[16:19], v[66:69], v[86:89], a[16:19]
	ds_read_b128 v[38:41], v164 offset:1024
	v_mfma_f32_16x16x32_f16 a[28:31], v[58:61], v[82:85], a[28:31]
	ds_read_b128 v[34:37], v164 offset:2048
	v_mfma_f32_16x16x32_f16 a[60:63], v[58:61], v[86:89], a[60:63]
	ds_read_b128 v[30:33], v164 offset:3072
	v_mfma_f32_16x16x32_f16 a[8:11], v[54:57], v[82:85], a[8:11]
	ds_read_b128 v[26:29], v164 offset:4096
	v_mfma_f32_16x16x32_f16 a[20:23], v[54:57], v[86:89], a[20:23]
	ds_read_b128 v[22:25], v164 offset:5120
	v_mfma_f32_16x16x32_f16 a[24:27], v[46:49], v[82:85], a[24:27]
	ds_read_b128 v[10:13], v164 offset:6144
	v_mfma_f32_16x16x32_f16 a[36:39], v[46:49], v[86:89], a[36:39]
	ds_read_b128 v[6:9], v164 offset:7168
	v_mfma_f32_16x16x32_f16 a[44:47], v[50:53], v[82:85], a[44:47]
	ds_read_b128 v[2:5], v164 offset:8192
	v_mfma_f32_16x16x32_f16 a[64:67], v[50:53], v[86:89], a[64:67]
	v_mfma_f32_16x16x32_f16 a[32:35], v[62:65], v[82:85], a[32:35]
	v_mfma_f32_16x16x32_f16 a[40:43], v[62:65], v[86:89], a[40:43]
	v_mfma_f32_16x16x32_f16 a[48:51], v[74:77], v[82:85], a[48:51]
	v_mfma_f32_16x16x32_f16 a[52:55], v[74:77], v[86:89], a[52:55]
	v_mfma_f32_16x16x32_f16 a[56:59], v[78:81], v[82:85], a[56:59]
	v_mfma_f32_16x16x32_f16 a[68:71], v[78:81], v[86:89], a[68:71]
	s_waitcnt lgkmcnt(8)
	v_mfma_f32_16x16x32_f16 a[0:3], v[42:45], v[14:17], a[0:3]
	ds_read_b128 v[82:85], v153
	v_mfma_f32_16x16x32_f16 a[4:7], v[42:45], v[18:21], a[4:7]
	ds_read_b128 v[86:89], v155
	s_waitcnt lgkmcnt(9)
	v_mfma_f32_16x16x32_f16 a[12:15], v[38:41], v[14:17], a[12:15]
	ds_read_b128 v[70:73], v164 offset:9216
	v_mfma_f32_16x16x32_f16 a[16:19], v[38:41], v[18:21], a[16:19]
	ds_read_b128 v[66:69], v164 offset:10240
	s_waitcnt lgkmcnt(10)
	v_mfma_f32_16x16x32_f16 a[28:31], v[34:37], v[14:17], a[28:31]
	ds_read_b128 v[58:61], v164 offset:11264
	v_mfma_f32_16x16x32_f16 a[60:63], v[34:37], v[18:21], a[60:63]
	ds_read_b128 v[54:57], v164 offset:12288
	s_waitcnt lgkmcnt(11)
	v_mfma_f32_16x16x32_f16 a[8:11], v[30:33], v[14:17], a[8:11]
	ds_read_b128 v[46:49], v164 offset:13312
	v_mfma_f32_16x16x32_f16 a[20:23], v[30:33], v[18:21], a[20:23]
	ds_read_b128 v[50:53], v164 offset:14336
	s_waitcnt lgkmcnt(12)
	v_mfma_f32_16x16x32_f16 a[24:27], v[26:29], v[14:17], a[24:27]
	ds_read_b128 v[62:65], v164 offset:15360
	v_mfma_f32_16x16x32_f16 a[36:39], v[26:29], v[18:21], a[36:39]
	ds_read_b128 v[74:77], v164 offset:16384
	s_waitcnt lgkmcnt(13)
	v_mfma_f32_16x16x32_f16 a[44:47], v[22:25], v[14:17], a[44:47]
	ds_read_b128 v[78:81], v164 offset:17408
	v_mfma_f32_16x16x32_f16 a[64:67], v[22:25], v[18:21], a[64:67]
	s_waitcnt lgkmcnt(13)
	v_mfma_f32_16x16x32_f16 a[32:35], v[10:13], v[14:17], a[32:35]
	v_mfma_f32_16x16x32_f16 a[40:43], v[10:13], v[18:21], a[40:43]
	s_waitcnt lgkmcnt(12)
	v_mfma_f32_16x16x32_f16 a[48:51], v[6:9], v[14:17], a[48:51]
	v_mfma_f32_16x16x32_f16 a[52:55], v[6:9], v[18:21], a[52:55]
	s_waitcnt lgkmcnt(11)
	v_mfma_f32_16x16x32_f16 a[56:59], v[2:5], v[14:17], a[56:59]
	v_mfma_f32_16x16x32_f16 a[68:71], v[2:5], v[18:21], a[68:71]
	s_waitcnt lgkmcnt(8)
	v_mfma_f32_16x16x32_f16 a[0:3], v[70:73], v[82:85], a[0:3]
	ds_read_b128 v[14:17], v156
	v_mfma_f32_16x16x32_f16 a[4:7], v[70:73], v[86:89], a[4:7]
	ds_read_b128 v[18:21], v158
	s_waitcnt lgkmcnt(9)
	v_mfma_f32_16x16x32_f16 a[12:15], v[66:69], v[82:85], a[12:15]
	ds_read_b128 v[42:45], v165
	v_mfma_f32_16x16x32_f16 a[16:19], v[66:69], v[86:89], a[16:19]
	ds_read_b128 v[38:41], v165 offset:1024
	s_waitcnt lgkmcnt(10)
	v_mfma_f32_16x16x32_f16 a[28:31], v[58:61], v[82:85], a[28:31]
	ds_read_b128 v[34:37], v165 offset:2048
	v_mfma_f32_16x16x32_f16 a[60:63], v[58:61], v[86:89], a[60:63]
	ds_read_b128 v[30:33], v165 offset:3072
	s_waitcnt lgkmcnt(11)
	v_mfma_f32_16x16x32_f16 a[8:11], v[54:57], v[82:85], a[8:11]
	ds_read_b128 v[26:29], v165 offset:4096
	v_mfma_f32_16x16x32_f16 a[20:23], v[54:57], v[86:89], a[20:23]
	ds_read_b128 v[22:25], v165 offset:5120
	s_waitcnt lgkmcnt(12)
	v_mfma_f32_16x16x32_f16 a[24:27], v[46:49], v[82:85], a[24:27]
	ds_read_b128 v[10:13], v165 offset:6144
	v_mfma_f32_16x16x32_f16 a[36:39], v[46:49], v[86:89], a[36:39]
	ds_read_b128 v[6:9], v165 offset:7168
	s_waitcnt lgkmcnt(13)
	v_mfma_f32_16x16x32_f16 a[44:47], v[50:53], v[82:85], a[44:47]
	ds_read_b128 v[2:5], v165 offset:8192
	v_mfma_f32_16x16x32_f16 a[64:67], v[50:53], v[86:89], a[64:67]
	s_waitcnt lgkmcnt(13)
	v_mfma_f32_16x16x32_f16 a[32:35], v[62:65], v[82:85], a[32:35]
	v_mfma_f32_16x16x32_f16 a[40:43], v[62:65], v[86:89], a[40:43]
	s_waitcnt lgkmcnt(12)
	v_mfma_f32_16x16x32_f16 a[48:51], v[74:77], v[82:85], a[48:51]
	v_mfma_f32_16x16x32_f16 a[52:55], v[74:77], v[86:89], a[52:55]
	s_waitcnt lgkmcnt(11)
	v_mfma_f32_16x16x32_f16 a[56:59], v[78:81], v[82:85], a[56:59]
	v_mfma_f32_16x16x32_f16 a[68:71], v[78:81], v[86:89], a[68:71]
	s_waitcnt lgkmcnt(8)
	v_mfma_f32_16x16x32_f16 a[0:3], v[42:45], v[14:17], a[0:3]
	ds_read_b128 v[82:85], v157
	v_mfma_f32_16x16x32_f16 a[4:7], v[42:45], v[18:21], a[4:7]
	ds_read_b128 v[86:89], v159
	s_waitcnt lgkmcnt(9)
	v_mfma_f32_16x16x32_f16 a[12:15], v[38:41], v[14:17], a[12:15]
	ds_read_b128 v[70:73], v165 offset:9216
	v_mfma_f32_16x16x32_f16 a[16:19], v[38:41], v[18:21], a[16:19]
	ds_read_b128 v[66:69], v165 offset:10240
	s_waitcnt lgkmcnt(10)
	v_mfma_f32_16x16x32_f16 a[28:31], v[34:37], v[14:17], a[28:31]
	ds_read_b128 v[58:61], v165 offset:11264
	v_mfma_f32_16x16x32_f16 a[60:63], v[34:37], v[18:21], a[60:63]
	ds_read_b128 v[54:57], v165 offset:12288
	s_waitcnt lgkmcnt(11)
	v_mfma_f32_16x16x32_f16 a[8:11], v[30:33], v[14:17], a[8:11]
	ds_read_b128 v[46:49], v165 offset:13312
	v_mfma_f32_16x16x32_f16 a[20:23], v[30:33], v[18:21], a[20:23]
	ds_read_b128 v[50:53], v165 offset:14336
	s_waitcnt lgkmcnt(12)
	v_mfma_f32_16x16x32_f16 a[24:27], v[26:29], v[14:17], a[24:27]
	ds_read_b128 v[62:65], v165 offset:15360
	v_mfma_f32_16x16x32_f16 a[36:39], v[26:29], v[18:21], a[36:39]
	ds_read_b128 v[74:77], v165 offset:16384
	s_waitcnt lgkmcnt(13)
	v_mfma_f32_16x16x32_f16 a[44:47], v[22:25], v[14:17], a[44:47]
	ds_read_b128 v[78:81], v165 offset:17408
	v_mfma_f32_16x16x32_f16 a[64:67], v[22:25], v[18:21], a[64:67]
	s_waitcnt lgkmcnt(13)
	v_mfma_f32_16x16x32_f16 a[32:35], v[10:13], v[14:17], a[32:35]
	v_mfma_f32_16x16x32_f16 a[40:43], v[10:13], v[18:21], a[40:43]
	s_waitcnt lgkmcnt(12)
	v_mfma_f32_16x16x32_f16 a[48:51], v[6:9], v[14:17], a[48:51]
	v_mfma_f32_16x16x32_f16 a[52:55], v[6:9], v[18:21], a[52:55]
	s_waitcnt lgkmcnt(11)
	v_mfma_f32_16x16x32_f16 a[56:59], v[2:5], v[14:17], a[56:59]
	v_mfma_f32_16x16x32_f16 a[68:71], v[2:5], v[18:21], a[68:71]
	s_waitcnt vmcnt(8) lgkmcnt(0)
	s_barrier
	s_add_u32 s52, s50, 0x24000
	s_addc_u32 s53, s51, 0
	s_add_i32 m0, s42, 0xc600
	s_nop 0
	global_load_lds_dwordx4 v137, s[52:53]
	s_add_i32 m0, s43, 0xc600
	s_nop 0
	global_load_lds_dwordx4 v138, s[52:53]
	s_cmp_lt_u32 s42, 0x800
	s_cbranch_scc0 .Lk4_st6_8
	s_add_i32 m0, s44, 0xc600
	s_nop 0
	global_load_lds_dwordx4 v139, s[52:53]
.Lk4_st6_8:
	s_add_u32 s52, s10, 0x800000
	s_addc_u32 s53, s11, 0
	v_lshlrev_b32_e32 v169, 2, v94
	v_readfirstlane_b32 s14, v118
	s_mov_b32 m0, s14
	s_nop 0
	global_load_lds_dwordx4 v169, s[52:53] nt
	v_lshlrev_b32_e32 v169, 2, v96
	v_readfirstlane_b32 s14, v90
	s_mov_b32 m0, s14
	s_nop 0
	global_load_lds_dwordx4 v169, s[52:53] nt
	v_mfma_f32_16x16x32_f16 a[0:3], v[70:73], v[82:85], a[0:3]
	ds_read_b128 v[14:17], v158
	v_mfma_f32_16x16x32_f16 a[4:7], v[70:73], v[86:89], a[4:7]
	ds_read_b128 v[18:21], v160
	v_mfma_f32_16x16x32_f16 a[12:15], v[66:69], v[82:85], a[12:15]
	ds_read_b128 v[42:45], v168
	v_mfma_f32_16x16x32_f16 a[16:19], v[66:69], v[86:89], a[16:19]
	ds_read_b128 v[38:41], v168 offset:1024
	v_mfma_f32_16x16x32_f16 a[28:31], v[58:61], v[82:85], a[28:31]
	ds_read_b128 v[34:37], v168 offset:2048
	v_mfma_f32_16x16x32_f16 a[60:63], v[58:61], v[86:89], a[60:63]
	ds_read_b128 v[30:33], v168 offset:3072
	v_mfma_f32_16x16x32_f16 a[8:11], v[54:57], v[82:85], a[8:11]
	ds_read_b128 v[26:29], v168 offset:4096
	v_mfma_f32_16x16x32_f16 a[20:23], v[54:57], v[86:89], a[20:23]
	ds_read_b128 v[22:25], v168 offset:5120
	v_mfma_f32_16x16x32_f16 a[24:27], v[46:49], v[82:85], a[24:27]
	ds_read_b128 v[10:13], v168 offset:6144
	v_mfma_f32_16x16x32_f16 a[36:39], v[46:49], v[86:89], a[36:39]
	ds_read_b128 v[6:9], v168 offset:7168
	v_mfma_f32_16x16x32_f16 a[44:47], v[50:53], v[82:85], a[44:47]
	ds_read_b128 v[2:5], v168 offset:8192
	v_mfma_f32_16x16x32_f16 a[64:67], v[50:53], v[86:89], a[64:67]
	v_mfma_f32_16x16x32_f16 a[32:35], v[62:65], v[82:85], a[32:35]
	v_mfma_f32_16x16x32_f16 a[40:43], v[62:65], v[86:89], a[40:43]
	v_mfma_f32_16x16x32_f16 a[48:51], v[74:77], v[82:85], a[48:51]
	v_mfma_f32_16x16x32_f16 a[52:55], v[74:77], v[86:89], a[52:55]
	v_mfma_f32_16x16x32_f16 a[56:59], v[78:81], v[82:85], a[56:59]
	v_mfma_f32_16x16x32_f16 a[68:71], v[78:81], v[86:89], a[68:71]
	s_waitcnt lgkmcnt(8)
	v_mfma_f32_16x16x32_f16 a[0:3], v[42:45], v[14:17], a[0:3]
	ds_read_b128 v[82:85], v159
	v_mfma_f32_16x16x32_f16 a[4:7], v[42:45], v[18:21], a[4:7]
	ds_read_b128 v[86:89], v161
	s_waitcnt lgkmcnt(9)
	v_mfma_f32_16x16x32_f16 a[12:15], v[38:41], v[14:17], a[12:15]
	ds_read_b128 v[70:73], v168 offset:9216
	v_mfma_f32_16x16x32_f16 a[16:19], v[38:41], v[18:21], a[16:19]
	ds_read_b128 v[66:69], v168 offset:10240
	s_waitcnt lgkmcnt(10)
	v_mfma_f32_16x16x32_f16 a[28:31], v[34:37], v[14:17], a[28:31]
	ds_read_b128 v[58:61], v168 offset:11264
	v_mfma_f32_16x16x32_f16 a[60:63], v[34:37], v[18:21], a[60:63]
	ds_read_b128 v[54:57], v168 offset:12288
	s_waitcnt lgkmcnt(11)
	v_mfma_f32_16x16x32_f16 a[8:11], v[30:33], v[14:17], a[8:11]
	ds_read_b128 v[46:49], v168 offset:13312
	v_mfma_f32_16x16x32_f16 a[20:23], v[30:33], v[18:21], a[20:23]
	ds_read_b128 v[50:53], v168 offset:14336
	s_waitcnt lgkmcnt(12)
	v_mfma_f32_16x16x32_f16 a[24:27], v[26:29], v[14:17], a[24:27]
	ds_read_b128 v[62:65], v168 offset:15360
	v_mfma_f32_16x16x32_f16 a[36:39], v[26:29], v[18:21], a[36:39]
	ds_read_b128 v[74:77], v168 offset:16384
	s_waitcnt lgkmcnt(13)
	v_mfma_f32_16x16x32_f16 a[44:47], v[22:25], v[14:17], a[44:47]
	ds_read_b128 v[78:81], v168 offset:17408
	v_mfma_f32_16x16x32_f16 a[64:67], v[22:25], v[18:21], a[64:67]
	s_waitcnt lgkmcnt(13)
	v_mfma_f32_16x16x32_f16 a[32:35], v[10:13], v[14:17], a[32:35]
	v_mfma_f32_16x16x32_f16 a[40:43], v[10:13], v[18:21], a[40:43]
	s_waitcnt lgkmcnt(12)
	v_mfma_f32_16x16x32_f16 a[48:51], v[6:9], v[14:17], a[48:51]
	v_mfma_f32_16x16x32_f16 a[52:55], v[6:9], v[18:21], a[52:55]
	s_waitcnt lgkmcnt(11)
	v_mfma_f32_16x16x32_f16 a[56:59], v[2:5], v[14:17], a[56:59]
	v_mfma_f32_16x16x32_f16 a[68:71], v[2:5], v[18:21], a[68:71]
	s_waitcnt vmcnt(2) lgkmcnt(0)
	s_barrier
	v_add_u32_e32 v169, s16, v118
	s_nop 1
	v_readfirstlane_b32 s14, v169
	s_mov_b32 m0, s14
	s_nop 0
	global_load_lds_dwordx4 v[0:1], off nt
	v_add_u32_e32 v169, s16, v90
	s_nop 1
	v_readfirstlane_b32 s14, v169
	s_mov_b32 m0, s14
	s_nop 0
	global_load_lds_dwordx4 v[106:107], off nt
	v_add_u32_e32 v169, s16, v91
	s_nop 1
	v_readfirstlane_b32 s14, v169
	s_mov_b32 m0, s14
	s_nop 0
	global_load_lds_dwordx4 v[110:111], off nt
	v_add_u32_e32 v169, s16, v119
	s_nop 1
	v_readfirstlane_b32 s14, v169
	s_mov_b32 m0, s14
	s_nop 0
	global_load_lds_dwordx4 v[114:115], off nt
	v_mfma_f32_16x16x32_f16 a[0:3], v[70:73], v[82:85], a[0:3]
	ds_read_b128 v[14:17], v160
	v_mfma_f32_16x16x32_f16 a[4:7], v[70:73], v[86:89], a[4:7]
	ds_read_b128 v[18:21], v162
	v_mfma_f32_16x16x32_f16 a[12:15], v[66:69], v[82:85], a[12:15]
	ds_read_b128 v[42:45], v164
	v_mfma_f32_16x16x32_f16 a[16:19], v[66:69], v[86:89], a[16:19]
	ds_read_b128 v[38:41], v164 offset:1024
	v_mfma_f32_16x16x32_f16 a[28:31], v[58:61], v[82:85], a[28:31]
	ds_read_b128 v[34:37], v164 offset:2048
	v_mfma_f32_16x16x32_f16 a[60:63], v[58:61], v[86:89], a[60:63]
	ds_read_b128 v[30:33], v164 offset:3072
	v_mfma_f32_16x16x32_f16 a[8:11], v[54:57], v[82:85], a[8:11]
	ds_read_b128 v[26:29], v164 offset:4096
	v_mfma_f32_16x16x32_f16 a[20:23], v[54:57], v[86:89], a[20:23]
	ds_read_b128 v[22:25], v164 offset:5120
	v_mfma_f32_16x16x32_f16 a[24:27], v[46:49], v[82:85], a[24:27]
	ds_read_b128 v[10:13], v164 offset:6144
	v_mfma_f32_16x16x32_f16 a[36:39], v[46:49], v[86:89], a[36:39]
	ds_read_b128 v[6:9], v164 offset:7168
	v_mfma_f32_16x16x32_f16 a[44:47], v[50:53], v[82:85], a[44:47]
	ds_read_b128 v[2:5], v164 offset:8192
	v_mfma_f32_16x16x32_f16 a[64:67], v[50:53], v[86:89], a[64:67]
	v_mfma_f32_16x16x32_f16 a[32:35], v[62:65], v[82:85], a[32:35]
	v_mfma_f32_16x16x32_f16 a[40:43], v[62:65], v[86:89], a[40:43]
	v_mfma_f32_16x16x32_f16 a[48:51], v[74:77], v[82:85], a[48:51]
	v_mfma_f32_16x16x32_f16 a[52:55], v[74:77], v[86:89], a[52:55]
	v_mfma_f32_16x16x32_f16 a[56:59], v[78:81], v[82:85], a[56:59]
	v_mfma_f32_16x16x32_f16 a[68:71], v[78:81], v[86:89], a[68:71]
	s_waitcnt lgkmcnt(8)
	v_mfma_f32_16x16x32_f16 a[0:3], v[42:45], v[14:17], a[0:3]
	ds_read_b128 v[82:85], v161
	v_mfma_f32_16x16x32_f16 a[4:7], v[42:45], v[18:21], a[4:7]
	ds_read_b128 v[86:89], v163
	s_waitcnt lgkmcnt(9)
	v_mfma_f32_16x16x32_f16 a[12:15], v[38:41], v[14:17], a[12:15]
	ds_read_b128 v[70:73], v164 offset:9216
	v_mfma_f32_16x16x32_f16 a[16:19], v[38:41], v[18:21], a[16:19]
	ds_read_b128 v[66:69], v164 offset:10240
	s_waitcnt lgkmcnt(10)
	v_mfma_f32_16x16x32_f16 a[28:31], v[34:37], v[14:17], a[28:31]
	ds_read_b128 v[58:61], v164 offset:11264
	v_mfma_f32_16x16x32_f16 a[60:63], v[34:37], v[18:21], a[60:63]
	ds_read_b128 v[54:57], v164 offset:12288
	s_waitcnt lgkmcnt(11)
	v_mfma_f32_16x16x32_f16 a[8:11], v[30:33], v[14:17], a[8:11]
	ds_read_b128 v[46:49], v164 offset:13312
	v_mfma_f32_16x16x32_f16 a[20:23], v[30:33], v[18:21], a[20:23]
	ds_read_b128 v[50:53], v164 offset:14336
	s_waitcnt lgkmcnt(12)
	v_mfma_f32_16x16x32_f16 a[24:27], v[26:29], v[14:17], a[24:27]
	ds_read_b128 v[62:65], v164 offset:15360
	v_mfma_f32_16x16x32_f16 a[36:39], v[26:29], v[18:21], a[36:39]
	ds_read_b128 v[74:77], v164 offset:16384
	s_waitcnt lgkmcnt(13)
	v_mfma_f32_16x16x32_f16 a[44:47], v[22:25], v[14:17], a[44:47]
	ds_read_b128 v[78:81], v164 offset:17408
	v_mfma_f32_16x16x32_f16 a[64:67], v[22:25], v[18:21], a[64:67]
	s_waitcnt lgkmcnt(13)
	v_mfma_f32_16x16x32_f16 a[32:35], v[10:13], v[14:17], a[32:35]
	v_mfma_f32_16x16x32_f16 a[40:43], v[10:13], v[18:21], a[40:43]
	s_waitcnt lgkmcnt(12)
	v_mfma_f32_16x16x32_f16 a[48:51], v[6:9], v[14:17], a[48:51]
	v_mfma_f32_16x16x32_f16 a[52:55], v[6:9], v[18:21], a[52:55]
	s_waitcnt lgkmcnt(11)
	v_mfma_f32_16x16x32_f16 a[56:59], v[2:5], v[14:17], a[56:59]
	v_mfma_f32_16x16x32_f16 a[68:71], v[2:5], v[18:21], a[68:71]
	s_waitcnt lgkmcnt(8)
	v_mfma_f32_16x16x32_f16 a[0:3], v[70:73], v[82:85], a[0:3]
	v_mfma_f32_16x16x32_f16 a[4:7], v[70:73], v[86:89], a[4:7]
	s_waitcnt lgkmcnt(9)
	v_mfma_f32_16x16x32_f16 a[12:15], v[66:69], v[82:85], a[12:15]
	v_mfma_f32_16x16x32_f16 a[16:19], v[66:69], v[86:89], a[16:19]
	s_waitcnt lgkmcnt(10)
	v_mfma_f32_16x16x32_f16 a[28:31], v[58:61], v[82:85], a[28:31]
	v_mfma_f32_16x16x32_f16 a[60:63], v[58:61], v[86:89], a[60:63]
	s_waitcnt lgkmcnt(11)
	v_mfma_f32_16x16x32_f16 a[8:11], v[54:57], v[82:85], a[8:11]
	v_mfma_f32_16x16x32_f16 a[20:23], v[54:57], v[86:89], a[20:23]
	s_waitcnt lgkmcnt(12)
	v_mfma_f32_16x16x32_f16 a[24:27], v[46:49], v[82:85], a[24:27]
	v_mfma_f32_16x16x32_f16 a[36:39], v[46:49], v[86:89], a[36:39]
	s_waitcnt lgkmcnt(13)
	v_mfma_f32_16x16x32_f16 a[44:47], v[50:53], v[82:85], a[44:47]
	v_mfma_f32_16x16x32_f16 a[64:67], v[50:53], v[86:89], a[64:67]
	s_waitcnt lgkmcnt(13)
	v_mfma_f32_16x16x32_f16 a[32:35], v[62:65], v[82:85], a[32:35]
	v_mfma_f32_16x16x32_f16 a[40:43], v[62:65], v[86:89], a[40:43]
	s_waitcnt lgkmcnt(12)
	v_mfma_f32_16x16x32_f16 a[48:51], v[74:77], v[82:85], a[48:51]
	v_mfma_f32_16x16x32_f16 a[52:55], v[74:77], v[86:89], a[52:55]
	s_waitcnt lgkmcnt(11)
	v_mfma_f32_16x16x32_f16 a[56:59], v[78:81], v[82:85], a[56:59]
	v_mfma_f32_16x16x32_f16 a[68:71], v[78:81], v[86:89], a[68:71]
	s_waitcnt lgkmcnt(0)
	s_setprio 0
.LBB3_32:
	s_barrier
	v_accvgpr_read_b32 v140, a72
	v_lshlrev_b64 v[142:143], 2, v[94:95]
	v_lshlrev_b64 v[144:145], 2, v[96:97]
	v_lshlrev_b64 v[146:147], 2, v[98:99]
	v_lshlrev_b64 v[148:149], 2, v[100:101]
	s_add_u32 s52, s10, 0x800000
	s_addc_u32 s53, s11, 0
	s_add_u32 s52, s10, 0xc00000
	s_addc_u32 s53, s11, 0
	v_add_u32_e32 v150, 0x7000, v91
	v_lshl_add_u64 v[152:153], s[52:53], 0, v[146:147]
	s_nop 0
	v_readfirstlane_b32 s44, v150
	s_mov_b32 m0, s44
	s_nop 0
	global_load_lds_dwordx4 v[152:153], off nt
	v_add_u32_e32 v150, 0x7000, v119
	v_lshl_add_u64 v[152:153], s[52:53], 0, v[148:149]
	s_nop 0
	v_readfirstlane_b32 s44, v150
	s_mov_b32 m0, s44
	s_nop 0
	global_load_lds_dwordx4 v[152:153], off nt
	s_add_u32 s52, s10, 0x1000000
	s_addc_u32 s53, s11, 0
	v_add_u32_e32 v150, 0xe000, v140
	v_lshl_add_u64 v[152:153], s[52:53], 0, v[142:143]
	s_nop 0
	v_readfirstlane_b32 s44, v150
	s_mov_b32 m0, s44
	s_nop 0
	global_load_lds_dwordx4 v[152:153], off nt
	v_add_u32_e32 v150, 0xe000, v90
	v_lshl_add_u64 v[152:153], s[52:53], 0, v[144:145]
	s_nop 0
	v_readfirstlane_b32 s44, v150
	s_mov_b32 m0, s44
	s_nop 0
	global_load_lds_dwordx4 v[152:153], off nt
	v_add_u32_e32 v150, 0xe000, v91
	v_lshl_add_u64 v[152:153], s[52:53], 0, v[146:147]
	s_nop 0
	v_readfirstlane_b32 s44, v150
	s_mov_b32 m0, s44
	s_nop 0
	global_load_lds_dwordx4 v[152:153], off nt
	v_add_u32_e32 v150, 0xe000, v119
	v_lshl_add_u64 v[152:153], s[52:53], 0, v[148:149]
	s_nop 0
	v_readfirstlane_b32 s44, v150
	s_mov_b32 m0, s44
	s_nop 0
	global_load_lds_dwordx4 v[152:153], off nt
	v_mbcnt_lo_u32_b32 v150, -1, 0
	v_mbcnt_hi_u32_b32 v150, -1, v150
	v_lshlrev_b32_e32 v150, 4, v150
	v_add_u32_e32 v151, v91, v150
	v_add_u32_e32 v152, v119, v150
	v_add_u32_e32 v153, v118, v150
	v_add_u32_e32 v154, v90, v150
	ds_write_b128 v151, v[128:131]
	ds_write_b128 v152, v[132:135]
	ds_write_b128 v153, v[172:175] offset:28672
	ds_write_b128 v154, v[176:179] offset:28672
	v_lshl_add_u32 v0, v120, 5, s22
	v_or_b32_e32 v1, s23, v121
	s_movk_i32 s0, 0x7f
	v_lshl_or_b32 v7, v93, 1, v0
	s_movk_i32 s1, 0x7e
	s_nop 15
	s_nop 15
	v_cmp_eq_u32_e64 s[4:5], s1, v7
	s_nop 7
	v_cmp_gt_u32_e32 vcc, s0, v1
	v_accvgpr_read_b32 v5, a14
	v_cmp_eq_u32_e64 s[0:1], 0, v1
	v_or_b32_e32 v4, v93, v7
	v_cmp_eq_u32_e64 s[2:3], 0, v4
	v_cndmask_b32_e64 v14, v5, 0, s[0:1]
	v_accvgpr_read_b32 v5, a13
	v_cndmask_b32_e64 v22, v5, 0, s[0:1]
	v_accvgpr_read_b32 v5, a12
	v_cndmask_b32_e64 v116, v5, 0, s[0:1]
	v_accvgpr_read_b32 v5, a49
	v_cndmask_b32_e32 v16, 0, v5, vcc
	v_accvgpr_read_b32 v5, a48
	v_cndmask_b32_e32 v28, 0, v5, vcc
	v_accvgpr_read_b32 v5, a30
	v_cndmask_b32_e64 v10, v5, 0, s[0:1]
	v_accvgpr_read_b32 v5, a29
	v_cndmask_b32_e64 v24, v5, 0, s[0:1]
	v_accvgpr_read_b32 v5, a28
	v_cndmask_b32_e64 v42, v5, 0, s[0:1]
	v_accvgpr_read_b32 v5, a57
	v_cndmask_b32_e32 v20, 0, v5, vcc
	v_accvgpr_read_b32 v5, a56
	v_cndmask_b32_e32 v38, 0, v5, vcc
	v_accvgpr_read_b32 v5, a6
	v_cndmask_b32_e64 v15, v5, 0, s[0:1]
	v_accvgpr_read_b32 v5, a5
	v_cndmask_b32_e64 v23, v5, 0, s[0:1]
	v_accvgpr_read_b32 v5, a4
	v_cndmask_b32_e64 v117, v5, 0, s[0:1]
	v_accvgpr_read_b32 v5, a41
	v_cndmask_b32_e32 v17, 0, v5, vcc
	v_accvgpr_read_b32 v5, a40
	v_cndmask_b32_e32 v29, 0, v5, vcc
	v_accvgpr_read_b32 v5, a17
	v_cndmask_b32_e64 v37, v5, 0, s[0:1]
	v_accvgpr_read_b32 v5, a16
	v_cndmask_b32_e64 v47, v5, 0, s[0:1]
	v_accvgpr_read_b32 v5, a52
	v_cndmask_b32_e32 v45, 0, v5, vcc
	v_accvgpr_read_b32 v5, a68
	v_cndmask_b32_e32 v12, 0, v5, vcc
	v_accvgpr_read_b32 v5, a0
	s_or_b64 s[8:9], s[2:3], s[0:1]
	v_cmp_eq_u32_e64 s[6:7], 15, v93
	v_accvgpr_read_b32 v11, a8
	v_cndmask_b32_e64 v112, v5, 0, s[8:9]
	v_accvgpr_read_b32 v4, a67
	v_mov_b32_e32 v5, 0x90
	s_and_b64 s[4:5], s[6:7], s[4:5]
	v_mov_b64_e32 v[40:41], v[16:17]
	v_cndmask_b32_e64 v16, v11, 0, s[2:3]
	v_cndmask_b32_e64 v11, 12, v5, s[6:7]
	v_cndmask_b32_e64 v61, v4, 0, s[4:5]
	v_accvgpr_read_b32 v4, a61
	s_or_b64 s[6:7], s[4:5], s[0:1]
	v_cndmask_b32_e64 v87, v4, 0, s[6:7]
	v_accvgpr_read_b32 v4, a60
	v_cndmask_b32_e64 v86, v4, 0, s[6:7]
	v_accvgpr_read_b32 v4, a65
	v_cndmask_b32_e64 v5, v4, 0, s[4:5]
	v_accvgpr_read_b32 v4, a64
	v_cndmask_b32_e64 v4, v4, 0, s[4:5]
	s_lshl_b32 s14, s18, 2
	v_mov_b64_e32 v[32:33], v[4:5]
	v_lshl_or_b32 v4, v122, 18, s14
	v_mov_b32_e32 v5, 0
	v_mov_b64_e32 v[62:63], v[14:15]
	v_lshl_add_u64 v[14:15], s[12:13], 0, v[4:5]
	v_lshlrev_b32_e32 v4, 7, v1
	v_lshl_add_u64 v[14:15], v[4:5], 2, v[14:15]
	v_lshlrev_b32_e32 v4, 2, v7
	v_mul_u32_u24_e32 v1, 24, v122
	v_lshl_add_u64 v[54:55], v[14:15], 0, v[4:5]
	v_mbcnt_lo_u32_b32 v138, -1, 0
	v_mbcnt_hi_u32_b32 v138, -1, v138
	v_and_b32_e32 v138, 1, v138
	v_mul_u32_u24_e32 v138, 0xfff8, v138
	v_add_u32_e32 v138, 0xffff0000, v138
	v_mov_b32_e32 v139, -1
	v_lshl_add_u64 v[134:135], v[54:55], 0, v[138:139]
	s_mov_b32 s28, 0x55555555
	s_mov_b32 s29, 0x55555555
	s_mov_b32 s30, 0xaaaaaaaa
	s_mov_b32 s31, 0xaaaaaaaa
	v_or_b32_e32 v1, v1, v121
	v_lshlrev_b32_e32 v4, 7, v120
	s_movk_i32 s12, 0x120
	v_mad_u32_u24 v1, v1, s12, v4
	s_add_u32 s12, s10, 0x800000
	v_accvgpr_read_b32 v7, a72
	v_mov_b64_e32 v[80:81], v[28:29]
	s_addc_u32 s13, s11, 0
	v_lshlrev_b64 v[28:29], 2, v[94:95]
	v_readfirstlane_b32 s14, v7
	v_add_u32_e32 v7, 0, v90
	v_lshl_add_u64 v[4:5], s[12:13], 0, v[28:29]
	s_mov_b32 m0, s14
	v_lshlrev_b64 v[30:31], 2, v[96:97]
	v_readfirstlane_b32 s14, v7
	v_mov_b32_e32 v14, v7
	v_add_u32_e32 v7, 0, v91
	s_waitcnt lgkmcnt(0)
	v_lshlrev_b64 v[56:57], 2, v[98:99]
	v_mov_b32_e32 v19, v7
	v_lshlrev_b64 v[58:59], 2, v[100:101]
	v_add_u32_e32 v7, 0, v119
	v_accvgpr_read_b32 v25, a72
	v_mov_b32_e32 v21, v7
	v_lshl_add_u32 v15, v93, 3, v1
	v_add_u32_e32 v1, v1, v11
	s_waitcnt vmcnt(16)
	v_accvgpr_write_b32 a12, v14
	v_mov_b64_e32 v[124:125], v[56:57]
	v_accvgpr_write_b32 a13, v19
	v_mov_b64_e32 v[126:127], v[58:59]
	v_accvgpr_write_b32 a16, v21
	s_waitcnt lgkmcnt(0)
	s_barrier
	v_add_u32_e32 v14, 0x16010, v15
	v_mov_b32_e32 v122, v15
	v_add_u32_e32 v15, 0x16000, v1
	ds_read_b64 v[64:65], v14
	ds_read_b64 v[66:67], v14 offset:288
	ds_read_b64 v[68:69], v14 offset:576
	ds_read_b64 v[76:77], v14 offset:1728
	ds_read_b64 v[78:79], v14 offset:2016
	ds_read_b64 v[4:5], v14 offset:2304
	ds_read_b64 v[84:85], v14 offset:3456
	ds_read_b64 v[74:75], v14 offset:3744
	ds_read_b64 v[88:89], v14 offset:4032
	ds_read_b64 v[100:101], v14 offset:5184
	ds_read_b64 v[106:107], v14 offset:5472
	ds_read_b64 v[120:121], v14 offset:5760
	ds_read_b32 v43, v15
	ds_read_b32 v19, v15 offset:288
	ds_read_b32 v39, v15 offset:576
	ds_read_b32 v25, v15 offset:1728
	ds_read_b32 v7, v15 offset:2016
	ds_read_b32 v21, v15 offset:2304
	ds_read_b32 v11, v15 offset:3456
	ds_read_b32 v35, v15 offset:3744
	ds_read_b32 v59, v15 offset:4032
	ds_read_b32 v57, v15 offset:5184
	ds_read_b32 v51, v15 offset:5472
	ds_read_b32 v49, v15 offset:5760
	s_waitcnt lgkmcnt(0)
	v_accvgpr_read_b32 v8, a26
	v_mov_b32_e32 v46, v43
	v_mov_b32_e32 v113, v65
	v_mov_b32_e32 v26, v19
	v_mov_b32_dpp v46, v65 row_shr:1 row_mask:0xf bank_mask:0xf
	v_pk_mul_f32 v[70:71], v[112:113], v[46:47]
	v_accvgpr_read_b32 v9, a22
	v_accvgpr_read_b32 v27, a36
	v_mov_b32_dpp v43, v64 row_shl:1 row_mask:0xf bank_mask:0xf
	v_mov_b32_dpp v26, v67 row_shr:1 row_mask:0xf bank_mask:0xf
	v_pk_fma_f32 v[70:71], v[64:65], v[116:117], v[70:71] op_sel_hi:[0,1,1]
	v_pk_mov_b32 v[64:65], v[64:65], v[86:87] op_sel:[1,0]
	v_mov_b32_e32 v17, v67
	v_mov_b64_e32 v[102:103], v[8:9]
	v_accvgpr_read_b32 v8, a25
	v_accvgpr_read_b32 v114, a24
	v_accvgpr_read_b32 v9, a21
	v_accvgpr_read_b32 v115, a20
	v_accvgpr_read_b32 v2, a32
	v_mov_b64_e32 v[82:83], v[30:31]
	v_pk_fma_f32 v[70:71], v[64:65], v[42:43], v[70:71]
	v_pk_mul_f32 v[64:65], v[16:17], v[26:27]
	v_mov_b64_e32 v[30:31], v[32:33]
	v_accvgpr_read_b32 v18, a44
	v_mov_b64_e32 v[104:105], v[8:9]
	v_cndmask_b32_e32 v9, 0, v2, vcc
	v_accvgpr_write_b32 a4, v14
	v_mov_b32_dpp v19, v66 row_shl:1 row_mask:0xf bank_mask:0xf
	v_pk_fma_f32 v[64:65], v[66:67], v[114:115], v[64:65] op_sel_hi:[0,1,1]
	v_pk_mov_b32 v[66:67], v[66:67], v[30:31] op_sel:[1,0]
	v_accvgpr_read_b32 v14, a69
	v_mov_b32_e32 v44, v39
	v_mov_b32_e32 v60, v1
	v_pk_fma_f32 v[66:67], v[66:67], v[18:19], v[64:65]
	v_cndmask_b32_e32 v14, 0, v14, vcc
	v_cndmask_b32_e64 v0, v9, 0, s[2:3]
	v_mov_b32_dpp v44, v69 row_shr:1 row_mask:0xf bank_mask:0xf
	v_pk_add_f32 v[70:71], v[70:71], 0 op_sel_hi:[1,0]
	v_mov_b32_e32 v1, v69
	v_accvgpr_write_b32 a0, v15
	v_cndmask_b32_e64 v15, v14, 0, s[4:5]
	v_cndmask_b32_e64 v14, v12, 0, s[4:5]
	v_pk_add_f32 v[66:67], v[70:71], v[66:67]
	v_pk_mul_f32 v[70:71], v[0:1], v[44:45]
	v_mov_b32_dpp v39, v68 row_shl:1 row_mask:0xf bank_mask:0xf
	v_pk_fma_f32 v[70:71], v[68:69], v[80:81], v[70:71] op_sel_hi:[0,1,1]
	v_pk_mov_b32 v[68:69], v[68:69], v[14:15] op_sel:[1,0]
	v_accvgpr_read_b32 v9, a1
	v_pk_fma_f32 v[68:69], v[68:69], v[38:39], v[70:71]
	v_mov_b32_e32 v36, v25
	v_cndmask_b32_e64 v64, v9, 0, s[8:9]
	v_pk_add_f32 v[66:67], v[66:67], v[68:69]
	v_mov_b32_dpp v36, v77 row_shr:1 row_mask:0xf bank_mask:0xf
	v_mov_b32_e32 v65, v77
	v_mov_b64_e32 v[108:109], v[22:23]
	v_accvgpr_read_b32 v9, a9
	v_mov_b32_e32 v128, v66
	v_mov_b32_e32 v129, v67
	v_mov_b32_e32 v12, v7
	v_pk_mul_f32 v[66:67], v[64:65], v[36:37]
	v_accvgpr_read_b32 v13, a37
	v_mov_b64_e32 v[72:73], v[28:29]
	v_cndmask_b32_e64 v28, v9, 0, s[2:3]
	v_mov_b32_dpp v25, v76 row_shl:1 row_mask:0xf bank_mask:0xf
	v_mov_b32_dpp v12, v79 row_shr:1 row_mask:0xf bank_mask:0xf
	v_pk_fma_f32 v[66:67], v[76:77], v[108:109], v[66:67] op_sel_hi:[0,1,1]
	v_mov_b32_e32 v76, v77
	v_mov_b32_e32 v77, v87
	v_mov_b32_e32 v29, v79
	v_pk_fma_f32 v[66:67], v[76:77], v[24:25], v[66:67]
	v_pk_mul_f32 v[76:77], v[28:29], v[12:13]
	v_accvgpr_read_b32 v6, a45
	v_accvgpr_read_b32 v2, a33
	v_mov_b32_dpp v7, v78 row_shl:1 row_mask:0xf bank_mask:0xf
	v_pk_fma_f32 v[76:77], v[78:79], v[104:105], v[76:77] op_sel_hi:[0,1,1]
	v_mov_b32_e32 v78, v79
	v_mov_b32_e32 v79, v31
	v_cndmask_b32_e32 v2, 0, v2, vcc
	v_accvgpr_read_b32 v50, a53
	v_pk_fma_f32 v[76:77], v[78:79], v[6:7], v[76:77]
	v_mov_b32_e32 v78, v21
	v_accvgpr_write_b32 a44, v80
	v_cndmask_b32_e32 v79, 0, v50, vcc
	v_cndmask_b32_e64 v52, v2, 0, s[2:3]
	v_mov_b32_dpp v78, v5 row_shr:1 row_mask:0xf bank_mask:0xf
	v_pk_add_f32 v[66:67], v[66:67], 0 op_sel_hi:[1,0]
	v_mov_b32_e32 v53, v5
	v_accvgpr_write_b32 a45, v81
	v_accvgpr_write_b32 a21, v15
	v_pk_add_f32 v[80:81], v[66:67], v[76:77]
	v_pk_mul_f32 v[66:67], v[52:53], v[78:79]
	v_accvgpr_write_b32 a24, v40
	v_accvgpr_read_b32 v2, a2
	v_mov_b32_dpp v21, v4 row_shl:1 row_mask:0xf bank_mask:0xf
	v_pk_fma_f32 v[66:67], v[4:5], v[40:41], v[66:67] op_sel_hi:[0,1,1]
	v_accvgpr_write_b32 a25, v41
	v_mov_b32_e32 v4, v5
	v_accvgpr_read_b32 v5, a21
	v_cndmask_b32_e64 v40, v2, 0, s[8:9]
	v_accvgpr_read_b32 v2, a62
	v_accvgpr_read_b32 v8, a18
	v_accvgpr_read_b32 v48, a63
	v_accvgpr_write_b32 a20, v14
	v_accvgpr_write_b32 a41, v23
	v_pk_fma_f32 v[4:5], v[4:5], v[20:21], v[66:67]
	s_mov_b64 s[12:13], 0x10000
	v_cndmask_b32_e64 v14, v2, 0, s[6:7]
	v_mov_b32_e32 v76, v11
	v_accvgpr_read_b32 v2, a10
	v_accvgpr_write_b32 a40, v22
	v_cndmask_b32_e64 v15, v48, 0, s[6:7]
	v_cndmask_b32_e64 v77, v8, 0, s[0:1]
	v_pk_add_f32 v[4:5], v[80:81], v[4:5]
	v_lshl_add_u64 v[136:137], v[134:135], 0, s[12:13]
	v_mov_b32_dpp v76, v85 row_shr:1 row_mask:0xf bank_mask:0xf
	v_mov_b32_e32 v41, v85
	v_cndmask_b32_e64 v22, v2, 0, s[2:3]
	v_mov_b32_e32 v2, v35
	v_accvgpr_read_b32 v1, a50
	v_accvgpr_read_b32 v3, a38
	s_mov_b64 s[32:33], vcc
	s_nop 1
	s_mov_b64 vcc, s[28:29]
	s_nop 0
	v_cndmask_b32_dpp v130, v4, v128, vcc quad_perm:[1,0,3,2] row_mask:0xf bank_mask:0xf
	v_cndmask_b32_dpp v131, v5, v129, vcc quad_perm:[1,0,3,2] row_mask:0xf bank_mask:0xf
	s_mov_b64 vcc, s[30:31]
	s_nop 0
	v_cndmask_b32_dpp v132, v128, v4, vcc quad_perm:[1,0,3,2] row_mask:0xf bank_mask:0xf
	v_cndmask_b32_dpp v133, v129, v5, vcc quad_perm:[1,0,3,2] row_mask:0xf bank_mask:0xf
	global_store_dwordx4 v[136:137], v[130:133], off sc0 sc1 nt
	s_nop 1
	s_mov_b64 vcc, s[32:33]
	v_mov_b64_e32 v[8:9], v[14:15]
	v_pk_mul_f32 v[4:5], v[40:41], v[76:77]
	v_mov_b64_e32 v[66:67], v[62:63]
	v_mov_b32_dpp v2, v75 row_shr:1 row_mask:0xf bank_mask:0xf
	v_mov_b32_e32 v23, v75
	v_cndmask_b32_e32 v62, 0, v1, vcc
	v_accvgpr_read_b32 v1, a42
	v_mov_b32_dpp v11, v84 row_shl:1 row_mask:0xf bank_mask:0xf
	v_pk_fma_f32 v[4:5], v[84:85], v[66:67], v[4:5] op_sel_hi:[0,1,1]
	v_pk_mov_b32 v[80:81], v[84:85], v[8:9] op_sel:[1,0]
	v_pk_mul_f32 v[84:85], v[22:23], v[2:3]
	v_accvgpr_read_b32 v2, a58
	v_cndmask_b32_e32 v63, 0, v1, vcc
	v_accvgpr_read_b32 v1, a70
	v_pk_fma_f32 v[80:81], v[80:81], v[10:11], v[4:5]
	v_accvgpr_read_b32 v4, a66
	v_cndmask_b32_e32 v58, 0, v2, vcc
	v_cndmask_b32_e32 v1, 0, v1, vcc
	v_accvgpr_read_b32 v2, a71
	v_cndmask_b32_e64 v8, v4, 0, s[4:5]
	v_cndmask_b32_e32 v2, 0, v2, vcc
	v_cndmask_b32_e64 v4, v1, 0, s[4:5]
	v_accvgpr_read_b32 v1, a34
	v_mov_b32_e32 v9, v61
	v_cndmask_b32_e64 v5, v2, 0, s[4:5]
	v_cndmask_b32_e32 v1, 0, v1, vcc
	v_accvgpr_read_b32 v2, a54
	v_mov_b32_e32 v92, v59
	v_accvgpr_read_b32 v34, a46
	v_mov_b32_dpp v35, v74 row_shl:1 row_mask:0xf bank_mask:0xf
	v_pk_fma_f32 v[84:85], v[74:75], v[102:103], v[84:85] op_sel_hi:[0,1,1]
	v_pk_mov_b32 v[74:75], v[74:75], v[8:9] op_sel:[1,0]
	v_cndmask_b32_e32 v93, 0, v2, vcc
	v_mov_b32_dpp v92, v89 row_shr:1 row_mask:0xf bank_mask:0xf
	v_cndmask_b32_e64 v96, v1, 0, s[2:3]
	v_mov_b32_e32 v97, v89
	v_accvgpr_read_b32 v1, a31
	v_pk_fma_f32 v[74:75], v[74:75], v[34:35], v[84:85]
	v_pk_mul_f32 v[84:85], v[96:97], v[92:93]
	v_accvgpr_write_b32 a8, v62
	v_cndmask_b32_e64 v56, v1, 0, s[0:1]
	v_accvgpr_read_b32 v1, a15
	v_pk_fma_f32 v[84:85], v[88:89], v[62:63], v[84:85] op_sel_hi:[0,1,1]
	v_accvgpr_write_b32 a9, v63
	v_cndmask_b32_e64 v62, v1, 0, s[0:1]
	v_accvgpr_read_b32 v1, a7
	v_cndmask_b32_e64 v63, v1, 0, s[0:1]
	v_accvgpr_read_b32 v1, a19
	v_pk_add_f32 v[80:81], v[80:81], 0 op_sel_hi:[1,0]
	v_mov_b32_dpp v59, v88 row_shl:1 row_mask:0xf bank_mask:0xf
	v_pk_mov_b32 v[88:89], v[88:89], v[4:5] op_sel:[1,0]
	v_cndmask_b32_e64 v95, v1, 0, s[0:1]
	v_accvgpr_read_b32 v1, a3
	v_accvgpr_write_b32 a36, v104
	v_pk_add_f32 v[80:81], v[80:81], v[74:75]
	v_pk_fma_f32 v[84:85], v[88:89], v[58:59], v[84:85]
	v_mov_b32_e32 v94, v57
	v_cndmask_b32_e64 v98, v1, 0, s[8:9]
	v_accvgpr_read_b32 v1, a11
	v_accvgpr_write_b32 a37, v105
	v_accvgpr_write_b32 a32, v102
	v_pk_add_f32 v[80:81], v[80:81], v[84:85]
	s_mov_b64 s[4:5], 0x20000
	v_mov_b32_dpp v94, v101 row_shr:1 row_mask:0xf bank_mask:0xf
	v_mov_b32_e32 v99, v101
	v_cndmask_b32_e64 v104, v1, 0, s[2:3]
	v_accvgpr_read_b32 v1, a59
	v_accvgpr_write_b32 a29, v15
	v_accvgpr_write_b32 a33, v103
	v_accvgpr_write_b32 a49, v5
	v_lshl_add_u64 v[84:85], v[54:55], 0, s[4:5]
	v_mov_b32_e32 v128, v80
	v_mov_b32_e32 v129, v81
	v_pk_mul_f32 v[80:81], v[98:99], v[94:95]
	v_mov_b32_e32 v102, v51
	v_cndmask_b32_e32 v48, 0, v1, vcc
	v_accvgpr_read_b32 v1, a51
	v_accvgpr_write_b32 a48, v4
	v_mov_b32_dpp v57, v100 row_shl:1 row_mask:0xf bank_mask:0xf
	v_pk_fma_f32 v[80:81], v[100:101], v[62:63], v[80:81] op_sel_hi:[0,1,1]
	v_mov_b32_e32 v84, v101
	v_accvgpr_read_b32 v85, a29
	v_accvgpr_read_b32 v103, a39
	v_mov_b32_dpp v102, v107 row_shr:1 row_mask:0xf bank_mask:0xf
	v_mov_b32_e32 v105, v107
	v_cndmask_b32_e32 v4, 0, v1, vcc
	v_accvgpr_read_b32 v1, a43
	v_pk_fma_f32 v[80:81], v[84:85], v[56:57], v[80:81]
	v_accvgpr_read_b32 v30, a27
	v_accvgpr_read_b32 v31, a23
	v_pk_mul_f32 v[84:85], v[104:105], v[102:103]
	v_cndmask_b32_e32 v5, 0, v1, vcc
	v_accvgpr_read_b32 v1, a35
	v_accvgpr_read_b32 v50, a47
	v_mov_b32_dpp v51, v106 row_shl:1 row_mask:0xf bank_mask:0xf
	v_pk_fma_f32 v[84:85], v[106:107], v[30:31], v[84:85] op_sel_hi:[0,1,1]
	v_mov_b32_e32 v106, v107
	v_mov_b32_e32 v107, v9
	v_cndmask_b32_e32 v1, 0, v1, vcc
	v_accvgpr_read_b32 v2, a55
	v_mov_b32_e32 v108, v49
	v_pk_fma_f32 v[84:85], v[106:107], v[50:51], v[84:85]
	v_pk_add_f32 v[80:81], v[80:81], 0 op_sel_hi:[1,0]
	v_cndmask_b32_e32 v109, 0, v2, vcc
	v_mov_b32_dpp v108, v121 row_shr:1 row_mask:0xf bank_mask:0xf
	v_cndmask_b32_e64 v110, v1, 0, s[2:3]
	v_mov_b32_e32 v111, v121
	v_pk_add_f32 v[80:81], v[80:81], v[84:85]
	v_pk_mul_f32 v[84:85], v[110:111], v[108:109]
	v_mov_b32_dpp v49, v120 row_shl:1 row_mask:0xf bank_mask:0xf
	v_pk_fma_f32 v[84:85], v[120:121], v[4:5], v[84:85] op_sel_hi:[0,1,1]
	v_mov_b32_e32 v120, v121
	v_accvgpr_read_b32 v121, a49
	v_pk_fma_f32 v[84:85], v[120:121], v[48:49], v[84:85]
	s_mov_b64 s[0:1], 0x30000
	v_pk_add_f32 v[80:81], v[80:81], v[84:85]
	v_lshl_add_u64 v[136:137], v[134:135], 0, s[0:1]
	v_add_u32_e32 v1, s17, v118
	s_add_u32 s0, s10, 0x1400000
	s_mov_b64 s[32:33], vcc
	s_nop 1
	s_mov_b64 vcc, s[28:29]
	s_nop 0
	v_cndmask_b32_dpp v130, v80, v128, vcc quad_perm:[1,0,3,2] row_mask:0xf bank_mask:0xf
	v_cndmask_b32_dpp v131, v81, v129, vcc quad_perm:[1,0,3,2] row_mask:0xf bank_mask:0xf
	s_mov_b64 vcc, s[30:31]
	s_nop 0
	v_cndmask_b32_dpp v132, v128, v80, vcc quad_perm:[1,0,3,2] row_mask:0xf bank_mask:0xf
	v_cndmask_b32_dpp v133, v129, v81, vcc quad_perm:[1,0,3,2] row_mask:0xf bank_mask:0xf
	global_store_dwordx4 v[136:137], v[130:133], off sc0 sc1 nt
	s_nop 1
	s_mov_b64 vcc, s[32:33]
	v_readfirstlane_b32 s2, v1
	s_addc_u32 s1, s11, 0
	v_add_u32_e32 v1, s17, v90
	s_waitcnt vmcnt(8)
	v_lshl_add_u64 v[80:81], s[0:1], 0, v[72:73]
	s_mov_b32 m0, s2
	v_readfirstlane_b32 s2, v1
	v_mov_b64_e32 v[74:75], v[82:83]
	v_add_u32_e32 v1, s17, v91
	s_waitcnt lgkmcnt(0)
	s_barrier
	global_load_lds_dwordx4 v[80:81], off nt
	v_lshl_add_u64 v[80:81], s[0:1], 0, v[74:75]
	s_mov_b32 m0, s2
	v_readfirstlane_b32 s2, v1
	v_add_u32_e32 v1, s17, v119
	global_load_lds_dwordx4 v[80:81], off nt
	v_lshl_add_u64 v[80:81], s[0:1], 0, v[124:125]
	s_mov_b32 m0, s2
	v_readfirstlane_b32 s2, v1
	global_load_lds_dwordx4 v[80:81], off nt
	v_lshl_add_u64 v[80:81], s[0:1], 0, v[126:127]
	s_mov_b32 m0, s2
	v_accvgpr_write_b32 a53, v33
	v_accvgpr_write_b32 a2, v62
	v_accvgpr_write_b32 a7, v5
	v_accvgpr_write_b32 a22, v124
	v_accvgpr_write_b32 a30, v126
	global_load_lds_dwordx4 v[80:81], off nt
	v_accvgpr_write_b32 a52, v32
	v_accvgpr_write_b32 a3, v63
	v_accvgpr_write_b32 a6, v4
	v_mov_b64_e32 v[32:33], v[72:73]
	v_accvgpr_write_b32 a23, v125
	v_accvgpr_write_b32 a31, v127
	v_add_u32_e32 v2, 0x1d010, v122
	v_accvgpr_write_b32 a10, v122
	v_add_u32_e32 v5, 0x1d000, v60
	v_mov_b32_e32 v4, v60
	ds_read_b64 v[62:63], v2
	ds_read_b64 v[60:61], v2 offset:288
	ds_read_b64 v[72:73], v2 offset:576
	ds_read_b64 v[70:71], v2 offset:1728
	ds_read_b64 v[68:69], v2 offset:2016
	ds_read_b64 v[82:83], v2 offset:2304
	ds_read_b64 v[80:81], v2 offset:3456
	ds_read_b64 v[84:85], v2 offset:3744
	ds_read_b64 v[126:127], v2 offset:4032
	ds_read_b64 v[124:125], v2 offset:5184
	ds_read_b64 v[122:123], v2 offset:5472
	ds_read_b64 v[120:121], v2 offset:5760
	ds_read_b32 v43, v5
	ds_read_b32 v19, v5 offset:288
	ds_read_b32 v39, v5 offset:576
	ds_read_b32 v25, v5 offset:1728
	ds_read_b32 v7, v5 offset:2016
	ds_read_b32 v21, v5 offset:2304
	ds_read_b32 v11, v5 offset:3456
	ds_read_b32 v35, v5 offset:3744
	ds_read_b32 v59, v5 offset:4032
	ds_read_b32 v57, v5 offset:5184
	ds_read_b32 v51, v5 offset:5472
	ds_read_b32 v49, v5 offset:5760
	s_waitcnt lgkmcnt(0)
	v_mov_b64_e32 v[100:101], v[86:87]
	v_mov_b32_e32 v46, v43
	v_mov_b32_e32 v113, v63
	v_mov_b32_e32 v26, v19
	v_mov_b32_dpp v46, v63 row_shr:1 row_mask:0xf bank_mask:0xf
	v_pk_mul_f32 v[88:89], v[112:113], v[46:47]
	v_mov_b32_dpp v43, v62 row_shl:1 row_mask:0xf bank_mask:0xf
	v_pk_fma_f32 v[88:89], v[62:63], v[116:117], v[88:89] op_sel_hi:[0,1,1]
	v_pk_mov_b32 v[62:63], v[62:63], v[100:101] op_sel:[1,0]
	v_mov_b32_dpp v26, v61 row_shr:1 row_mask:0xf bank_mask:0xf
	v_mov_b32_e32 v17, v61
	v_pk_fma_f32 v[62:63], v[62:63], v[42:43], v[88:89]
	v_pk_mul_f32 v[88:89], v[16:17], v[26:27]
	v_accvgpr_write_b32 a34, v16
	v_accvgpr_read_b32 v16, a52
	v_accvgpr_read_b32 v17, a53
	v_mov_b32_dpp v19, v60 row_shl:1 row_mask:0xf bank_mask:0xf
	v_pk_fma_f32 v[88:89], v[60:61], v[114:115], v[88:89] op_sel_hi:[0,1,1]
	v_pk_mov_b32 v[60:61], v[60:61], v[16:17] op_sel:[1,0]
	v_mov_b32_e32 v44, v39
	v_accvgpr_write_b32 a28, v14
	v_pk_fma_f32 v[60:61], v[60:61], v[18:19], v[88:89]
	v_pk_add_f32 v[62:63], v[62:63], 0 op_sel_hi:[1,0]
	v_mov_b32_dpp v44, v73 row_shr:1 row_mask:0xf bank_mask:0xf
	v_mov_b32_e32 v1, v73
	v_accvgpr_read_b32 v14, a44
	v_accvgpr_read_b32 v89, a21
	v_pk_add_f32 v[60:61], v[62:63], v[60:61]
	v_pk_mul_f32 v[62:63], v[0:1], v[44:45]
	v_accvgpr_read_b32 v15, a45
	v_accvgpr_read_b32 v88, a20
	v_mov_b32_dpp v39, v72 row_shl:1 row_mask:0xf bank_mask:0xf
	v_pk_fma_f32 v[62:63], v[72:73], v[14:15], v[62:63] op_sel_hi:[0,1,1]
	v_pk_mov_b32 v[72:73], v[72:73], v[88:89] op_sel:[1,0]
	v_mov_b32_e32 v36, v25
	v_pk_fma_f32 v[62:63], v[72:73], v[38:39], v[62:63]
	s_mov_b64 s[0:1], 0x400000
	v_pk_add_f32 v[60:61], v[60:61], v[62:63]
	v_mov_b32_dpp v36, v71 row_shr:1 row_mask:0xf bank_mask:0xf
	v_mov_b32_e32 v65, v71
	v_accvgpr_read_b32 v87, a41
	v_lshl_add_u64 v[62:63], v[54:55], 0, s[0:1]
	v_mov_b32_e32 v128, v60
	v_mov_b32_e32 v129, v61
	v_pk_mul_f32 v[60:61], v[64:65], v[36:37]
	v_accvgpr_read_b32 v86, a40
	v_mov_b32_e32 v12, v7
	v_mov_b32_dpp v25, v70 row_shl:1 row_mask:0xf bank_mask:0xf
	v_pk_fma_f32 v[60:61], v[70:71], v[86:87], v[60:61] op_sel_hi:[0,1,1]
	v_mov_b32_e32 v62, v71
	v_mov_b32_e32 v63, v101
	v_mov_b32_dpp v12, v69 row_shr:1 row_mask:0xf bank_mask:0xf
	v_mov_b32_e32 v29, v69
	v_accvgpr_read_b32 v107, a37
	v_pk_fma_f32 v[60:61], v[62:63], v[24:25], v[60:61]
	v_pk_mul_f32 v[62:63], v[28:29], v[12:13]
	v_accvgpr_read_b32 v106, a36
	v_mov_b32_dpp v7, v68 row_shl:1 row_mask:0xf bank_mask:0xf
	v_pk_fma_f32 v[62:63], v[68:69], v[106:107], v[62:63] op_sel_hi:[0,1,1]
	v_mov_b32_e32 v68, v69
	v_mov_b32_e32 v69, v17
	v_mov_b32_e32 v78, v21
	v_pk_fma_f32 v[62:63], v[68:69], v[6:7], v[62:63]
	v_pk_add_f32 v[60:61], v[60:61], 0 op_sel_hi:[1,0]
	v_mov_b32_dpp v78, v83 row_shr:1 row_mask:0xf bank_mask:0xf
	v_mov_b32_e32 v53, v83
	v_accvgpr_read_b32 v14, a24
	v_pk_add_f32 v[60:61], v[60:61], v[62:63]
	v_pk_mul_f32 v[62:63], v[52:53], v[78:79]
	v_accvgpr_read_b32 v15, a25
	v_mov_b32_dpp v21, v82 row_shl:1 row_mask:0xf bank_mask:0xf
	v_pk_fma_f32 v[62:63], v[82:83], v[14:15], v[62:63] op_sel_hi:[0,1,1]
	v_mov_b32_e32 v68, v83
	v_mov_b32_e32 v69, v89
	v_pk_fma_f32 v[62:63], v[68:69], v[20:21], v[62:63]
	v_mov_b32_e32 v76, v11
	v_pk_add_f32 v[60:61], v[60:61], v[62:63]
	s_mov_b64 s[0:1], 0x410000
	v_mov_b32_dpp v76, v81 row_shr:1 row_mask:0xf bank_mask:0xf
	v_mov_b32_e32 v41, v81
	v_lshl_add_u64 v[136:137], v[134:135], 0, s[0:1]
	s_nop 1
	s_mov_b64 vcc, s[28:29]
	s_nop 0
	v_cndmask_b32_dpp v130, v60, v128, vcc quad_perm:[1,0,3,2] row_mask:0xf bank_mask:0xf
	v_cndmask_b32_dpp v131, v61, v129, vcc quad_perm:[1,0,3,2] row_mask:0xf bank_mask:0xf
	s_mov_b64 vcc, s[30:31]
	s_nop 0
	v_cndmask_b32_dpp v132, v128, v60, vcc quad_perm:[1,0,3,2] row_mask:0xf bank_mask:0xf
	v_cndmask_b32_dpp v133, v129, v61, vcc quad_perm:[1,0,3,2] row_mask:0xf bank_mask:0xf
	global_store_dwordx4 v[136:137], v[130:133], off sc0 sc1 nt
	s_nop 1
	v_pk_mul_f32 v[60:61], v[40:41], v[76:77]
	v_accvgpr_write_b32 a36, v66
	v_pk_fma_f32 v[60:61], v[80:81], v[66:67], v[60:61] op_sel_hi:[0,1,1]
	v_accvgpr_write_b32 a37, v67
	v_accvgpr_read_b32 v67, a29
	v_accvgpr_write_b32 a5, v2
	v_accvgpr_write_b32 a38, v100
	v_accvgpr_read_b32 v66, a28
	v_mov_b32_e32 v2, v35
	v_accvgpr_write_b32 a39, v101
	v_mov_b32_dpp v11, v80 row_shl:1 row_mask:0xf bank_mask:0xf
	v_pk_mov_b32 v[62:63], v[80:81], v[66:67] op_sel:[1,0]
	v_mov_b32_dpp v2, v85 row_shr:1 row_mask:0xf bank_mask:0xf
	v_mov_b32_e32 v23, v85
	v_accvgpr_read_b32 v101, a33
	v_pk_fma_f32 v[60:61], v[62:63], v[10:11], v[60:61]
	v_pk_mul_f32 v[62:63], v[22:23], v[2:3]
	v_accvgpr_read_b32 v100, a32
	v_mov_b32_dpp v35, v84 row_shl:1 row_mask:0xf bank_mask:0xf
	v_pk_fma_f32 v[62:63], v[84:85], v[100:101], v[62:63] op_sel_hi:[0,1,1]
	v_pk_mov_b32 v[68:69], v[84:85], v[8:9] op_sel:[1,0]
	v_mov_b32_e32 v92, v59
	v_pk_fma_f32 v[62:63], v[68:69], v[34:35], v[62:63]
	v_pk_add_f32 v[60:61], v[60:61], 0 op_sel_hi:[1,0]
	v_mov_b32_dpp v92, v127 row_shr:1 row_mask:0xf bank_mask:0xf
	v_mov_b32_e32 v97, v127
	v_accvgpr_read_b32 v17, a9
	v_accvgpr_read_b32 v71, a49
	v_pk_add_f32 v[60:61], v[60:61], v[62:63]
	v_pk_mul_f32 v[62:63], v[96:97], v[92:93]
	v_accvgpr_read_b32 v16, a8
	v_accvgpr_read_b32 v70, a48
	v_mov_b32_dpp v59, v126 row_shl:1 row_mask:0xf bank_mask:0xf
	v_pk_fma_f32 v[62:63], v[126:127], v[16:17], v[62:63] op_sel_hi:[0,1,1]
	v_pk_mov_b32 v[68:69], v[126:127], v[70:71] op_sel:[1,0]
	v_mov_b32_e32 v94, v57
	v_pk_fma_f32 v[62:63], v[68:69], v[58:59], v[62:63]
	v_accvgpr_write_b32 a20, v28
	v_pk_add_f32 v[60:61], v[60:61], v[62:63]
	s_mov_b64 s[0:1], 0x420000
	v_mov_b32_dpp v94, v125 row_shr:1 row_mask:0xf bank_mask:0xf
	v_mov_b32_e32 v99, v125
	v_accvgpr_read_b32 v29, a3
	v_lshl_add_u64 v[62:63], v[54:55], 0, s[0:1]
	v_mov_b32_e32 v128, v60
	v_mov_b32_e32 v129, v61
	v_pk_mul_f32 v[60:61], v[98:99], v[94:95]
	v_accvgpr_read_b32 v28, a2
	v_mov_b32_e32 v102, v51
	v_mov_b32_dpp v57, v124 row_shl:1 row_mask:0xf bank_mask:0xf
	v_pk_fma_f32 v[60:61], v[124:125], v[28:29], v[60:61] op_sel_hi:[0,1,1]
	v_mov_b32_e32 v62, v125
	v_mov_b32_e32 v63, v67
	v_mov_b32_dpp v102, v123 row_shr:1 row_mask:0xf bank_mask:0xf
	v_mov_b32_e32 v105, v123
	v_pk_fma_f32 v[60:61], v[62:63], v[56:57], v[60:61]
	v_pk_mul_f32 v[62:63], v[104:105], v[102:103]
	v_mov_b32_dpp v51, v122 row_shl:1 row_mask:0xf bank_mask:0xf
	v_pk_fma_f32 v[62:63], v[122:123], v[30:31], v[62:63] op_sel_hi:[0,1,1]
	v_accvgpr_write_b32 a28, v30
	v_mov_b32_e32 v68, v123
	v_mov_b32_e32 v69, v9
	v_mov_b32_e32 v108, v49
	v_accvgpr_write_b32 a29, v31
	v_pk_fma_f32 v[62:63], v[68:69], v[50:51], v[62:63]
	v_pk_add_f32 v[60:61], v[60:61], 0 op_sel_hi:[1,0]
	v_mov_b32_dpp v108, v121 row_shr:1 row_mask:0xf bank_mask:0xf
	v_mov_b32_e32 v111, v121
	v_accvgpr_read_b32 v31, a7
	v_pk_add_f32 v[60:61], v[60:61], v[62:63]
	v_pk_mul_f32 v[62:63], v[110:111], v[108:109]
	v_accvgpr_read_b32 v30, a6
	v_mov_b32_dpp v49, v120 row_shl:1 row_mask:0xf bank_mask:0xf
	v_pk_fma_f32 v[62:63], v[120:121], v[30:31], v[62:63] op_sel_hi:[0,1,1]
	v_mov_b32_e32 v68, v121
	v_mov_b32_e32 v69, v71
	v_pk_fma_f32 v[62:63], v[68:69], v[48:49], v[62:63]
	s_mov_b64 s[0:1], 0x430000
	v_pk_add_f32 v[60:61], v[60:61], v[62:63]
	v_lshl_add_u64 v[136:137], v[134:135], 0, s[0:1]
	v_add_u32_e32 v1, s16, v118
	s_add_u32 s0, s10, 0x1800000
	v_accvgpr_write_b32 a26, v114
	s_nop 1
	s_mov_b64 vcc, s[28:29]
	s_nop 0
	v_cndmask_b32_dpp v130, v60, v128, vcc quad_perm:[1,0,3,2] row_mask:0xf bank_mask:0xf
	v_cndmask_b32_dpp v131, v61, v129, vcc quad_perm:[1,0,3,2] row_mask:0xf bank_mask:0xf
	s_mov_b64 vcc, s[30:31]
	s_nop 0
	v_cndmask_b32_dpp v132, v128, v60, vcc quad_perm:[1,0,3,2] row_mask:0xf bank_mask:0xf
	v_cndmask_b32_dpp v133, v129, v61, vcc quad_perm:[1,0,3,2] row_mask:0xf bank_mask:0xf
	global_store_dwordx4 v[136:137], v[130:133], off sc0 sc1 nt
	s_nop 1
	v_readfirstlane_b32 s2, v1
	s_addc_u32 s1, s11, 0
	v_add_u32_e32 v1, s16, v90
	v_accvgpr_write_b32 a18, v116
	v_accvgpr_write_b32 a27, v115
	s_waitcnt vmcnt(16)
	v_lshl_add_u64 v[60:61], s[0:1], 0, v[32:33]
	s_mov_b32 m0, s2
	v_readfirstlane_b32 s2, v1
	v_add_u32_e32 v1, s16, v91
	v_accvgpr_read_b32 v115, a23
	v_accvgpr_write_b32 a19, v117
	s_waitcnt lgkmcnt(0)
	s_barrier
	global_load_lds_dwordx4 v[60:61], off nt
	v_lshl_add_u64 v[60:61], s[0:1], 0, v[74:75]
	s_mov_b32 m0, s2
	v_readfirstlane_b32 s2, v1
	v_accvgpr_read_b32 v114, a22
	v_add_u32_e32 v1, s16, v119
	v_accvgpr_read_b32 v117, a31
	global_load_lds_dwordx4 v[60:61], off nt
	v_lshl_add_u64 v[60:61], s[0:1], 0, v[114:115]
	s_mov_b32 m0, s2
	v_readfirstlane_b32 s2, v1
	v_accvgpr_read_b32 v116, a30
	global_load_lds_dwordx4 v[60:61], off nt
	v_lshl_add_u64 v[60:61], s[0:1], 0, v[116:117]
	s_mov_b32 m0, s2
	v_accvgpr_write_b32 a1, v5
	global_load_lds_dwordx4 v[60:61], off nt
	v_accvgpr_read_b32 v5, a10
	v_add_u32_e32 v2, 16, v5
	ds_read_b64 v[60:61], v2
	ds_read_b64 v[62:63], v2 offset:288
	ds_read_b64 v[68:69], v2 offset:576
	ds_read_b64 v[70:71], v2 offset:1728
	ds_read_b64 v[72:73], v2 offset:2016
	ds_read_b64 v[82:83], v2 offset:2304
	ds_read_b64 v[80:81], v2 offset:3456
	ds_read_b64 v[84:85], v2 offset:3744
	ds_read_b64 v[124:125], v2 offset:4032
	ds_read_b64 v[122:123], v2 offset:5184
	ds_read_b64 v[120:121], v2 offset:5472
	ds_read_b64 v[90:91], v2 offset:5760
	ds_read_b32 v43, v4
	ds_read_b32 v19, v4 offset:288
	ds_read_b32 v39, v4 offset:576
	ds_read_b32 v25, v4 offset:1728
	ds_read_b32 v7, v4 offset:2016
	ds_read_b32 v21, v4 offset:2304
	ds_read_b32 v11, v4 offset:3456
	ds_read_b32 v35, v4 offset:3744
	ds_read_b32 v59, v4 offset:4032
	ds_read_b32 v57, v4 offset:5184
	ds_read_b32 v51, v4 offset:5472
	ds_read_b32 v49, v4 offset:5760
	s_waitcnt lgkmcnt(0)
	v_accvgpr_write_b32 a46, v88
	v_mov_b32_e32 v46, v43
	v_accvgpr_write_b32 a8, v8
	v_mov_b32_e32 v113, v61
	v_mov_b32_dpp v46, v61 row_shr:1 row_mask:0xf bank_mask:0xf
	v_accvgpr_mov_b32 a42, a52
	v_accvgpr_write_b32 a47, v89
	v_accvgpr_write_b32 a9, v9
	v_pk_mul_f32 v[88:89], v[112:113], v[46:47]
	v_accvgpr_write_b32 a40, v112
	v_accvgpr_read_b32 v8, a18
	v_accvgpr_read_b32 v113, a39
	v_accvgpr_mov_b32 a43, a53
	v_accvgpr_write_b32 a51, v33
	v_accvgpr_write_b32 a52, v74
	v_accvgpr_read_b32 v9, a19
	v_accvgpr_read_b32 v112, a38
	v_mov_b32_e32 v26, v19
	v_accvgpr_write_b32 a50, v32
	v_accvgpr_write_b32 a53, v75
	v_mov_b32_dpp v43, v60 row_shl:1 row_mask:0xf bank_mask:0xf
	v_pk_fma_f32 v[88:89], v[60:61], v[8:9], v[88:89] op_sel_hi:[0,1,1]
	v_pk_mov_b32 v[60:61], v[60:61], v[112:113] op_sel:[1,0]
	v_mov_b32_dpp v26, v63 row_shr:1 row_mask:0xf bank_mask:0xf
	v_accvgpr_read_b32 v32, a34
	v_mov_b32_e32 v33, v63
	v_accvgpr_read_b32 v127, a27
	v_accvgpr_read_b32 v75, a43
	v_pk_fma_f32 v[60:61], v[60:61], v[42:43], v[88:89]
	v_pk_mul_f32 v[88:89], v[32:33], v[26:27]
	v_accvgpr_read_b32 v126, a26
	v_accvgpr_read_b32 v74, a42
	v_mov_b32_dpp v19, v62 row_shl:1 row_mask:0xf bank_mask:0xf
	v_pk_fma_f32 v[88:89], v[62:63], v[126:127], v[88:89] op_sel_hi:[0,1,1]
	v_pk_mov_b32 v[62:63], v[62:63], v[74:75] op_sel:[1,0]
	v_mov_b32_e32 v44, v39
	v_accvgpr_mov_b32 a14, a48
	v_pk_fma_f32 v[62:63], v[62:63], v[18:19], v[88:89]
	v_pk_add_f32 v[60:61], v[60:61], 0 op_sel_hi:[1,0]
	v_mov_b32_dpp v44, v69 row_shr:1 row_mask:0xf bank_mask:0xf
	v_mov_b32_e32 v1, v69
	v_accvgpr_mov_b32 a15, a49
	v_pk_add_f32 v[60:61], v[60:61], v[62:63]
	v_pk_mul_f32 v[62:63], v[0:1], v[44:45]
	v_accvgpr_write_b32 a48, v0
	v_accvgpr_read_b32 v89, a45
	v_accvgpr_read_b32 v0, a46
	v_accvgpr_read_b32 v88, a44
	v_accvgpr_read_b32 v1, a47
	v_mov_b32_dpp v39, v68 row_shl:1 row_mask:0xf bank_mask:0xf
	v_pk_fma_f32 v[62:63], v[68:69], v[88:89], v[62:63] op_sel_hi:[0,1,1]
	v_pk_mov_b32 v[68:69], v[68:69], v[0:1] op_sel:[1,0]
	v_mov_b32_e32 v36, v25
	v_pk_fma_f32 v[62:63], v[68:69], v[38:39], v[62:63]
	s_mov_b64 s[0:1], 0x800000
	v_pk_add_f32 v[60:61], v[60:61], v[62:63]
	v_mov_b32_dpp v36, v71 row_shr:1 row_mask:0xf bank_mask:0xf
	v_mov_b32_e32 v65, v71
	v_lshl_add_u64 v[62:63], v[54:55], 0, s[0:1]
	v_mov_b32_e32 v128, v60
	v_mov_b32_e32 v129, v61
	v_pk_mul_f32 v[60:61], v[64:65], v[36:37]
	v_mov_b64_e32 v[118:119], v[86:87]
	v_mov_b32_e32 v12, v7
	v_accvgpr_write_b32 a24, v32
	v_mov_b32_dpp v25, v70 row_shl:1 row_mask:0xf bank_mask:0xf
	v_pk_fma_f32 v[60:61], v[70:71], v[118:119], v[60:61] op_sel_hi:[0,1,1]
	v_mov_b32_e32 v62, v71
	v_mov_b32_e32 v63, v113
	v_mov_b32_dpp v12, v73 row_shr:1 row_mask:0xf bank_mask:0xf
	v_accvgpr_read_b32 v32, a20
	v_mov_b32_e32 v33, v73
	v_pk_fma_f32 v[60:61], v[62:63], v[24:25], v[60:61]
	v_pk_mul_f32 v[62:63], v[32:33], v[12:13]
	v_mov_b32_dpp v7, v72 row_shl:1 row_mask:0xf bank_mask:0xf
	v_pk_fma_f32 v[62:63], v[72:73], v[106:107], v[62:63] op_sel_hi:[0,1,1]
	v_mov_b32_e32 v68, v73
	v_mov_b32_e32 v69, v75
	v_mov_b32_e32 v78, v21
	v_pk_fma_f32 v[62:63], v[68:69], v[6:7], v[62:63]
	v_pk_add_f32 v[60:61], v[60:61], 0 op_sel_hi:[1,0]
	v_mov_b32_dpp v78, v83 row_shr:1 row_mask:0xf bank_mask:0xf
	v_mov_b32_e32 v53, v83
	v_pk_add_f32 v[60:61], v[60:61], v[62:63]
	v_pk_mul_f32 v[62:63], v[52:53], v[78:79]
	v_mov_b32_dpp v21, v82 row_shl:1 row_mask:0xf bank_mask:0xf
	v_pk_fma_f32 v[62:63], v[82:83], v[14:15], v[62:63] op_sel_hi:[0,1,1]
	v_mov_b32_e32 v68, v83
	v_mov_b32_e32 v69, v1
	v_accvgpr_write_b32 a19, v15
	v_pk_fma_f32 v[62:63], v[68:69], v[20:21], v[62:63]
	v_mov_b32_e32 v76, v11
	v_accvgpr_write_b32 a18, v14
	v_pk_add_f32 v[60:61], v[60:61], v[62:63]
	s_mov_b64 s[0:1], 0x810000
	v_mov_b32_dpp v76, v81 row_shr:1 row_mask:0xf bank_mask:0xf
	v_mov_b32_e32 v41, v81
	v_accvgpr_read_b32 v14, a36
	v_accvgpr_write_b32 a6, v2
	v_lshl_add_u64 v[136:137], v[134:135], 0, s[0:1]
	s_nop 1
	s_mov_b64 vcc, s[28:29]
	s_nop 0
	v_cndmask_b32_dpp v130, v60, v128, vcc quad_perm:[1,0,3,2] row_mask:0xf bank_mask:0xf
	v_cndmask_b32_dpp v131, v61, v129, vcc quad_perm:[1,0,3,2] row_mask:0xf bank_mask:0xf
	s_mov_b64 vcc, s[30:31]
	s_nop 0
	v_cndmask_b32_dpp v132, v128, v60, vcc quad_perm:[1,0,3,2] row_mask:0xf bank_mask:0xf
	v_cndmask_b32_dpp v133, v129, v61, vcc quad_perm:[1,0,3,2] row_mask:0xf bank_mask:0xf
	global_store_dwordx4 v[136:137], v[130:133], off sc0 sc1 nt
	s_nop 1
	v_pk_mul_f32 v[60:61], v[40:41], v[76:77]
	v_accvgpr_read_b32 v15, a37
	v_mov_b32_e32 v2, v35
	v_mov_b32_dpp v11, v80 row_shl:1 row_mask:0xf bank_mask:0xf
	v_pk_fma_f32 v[60:61], v[80:81], v[14:15], v[60:61] op_sel_hi:[0,1,1]
	v_pk_mov_b32 v[62:63], v[80:81], v[66:67] op_sel:[1,0]
	v_mov_b32_dpp v2, v85 row_shr:1 row_mask:0xf bank_mask:0xf
	v_mov_b32_e32 v23, v85
	v_accvgpr_read_b32 v15, a9
	v_pk_fma_f32 v[60:61], v[62:63], v[10:11], v[60:61]
	v_pk_mul_f32 v[62:63], v[22:23], v[2:3]
	v_accvgpr_read_b32 v14, a8
	v_mov_b32_dpp v35, v84 row_shl:1 row_mask:0xf bank_mask:0xf
	v_pk_fma_f32 v[62:63], v[84:85], v[100:101], v[62:63] op_sel_hi:[0,1,1]
	v_pk_mov_b32 v[68:69], v[84:85], v[14:15] op_sel:[1,0]
	v_mov_b32_e32 v92, v59
	v_pk_fma_f32 v[62:63], v[68:69], v[34:35], v[62:63]
	v_pk_add_f32 v[60:61], v[60:61], 0 op_sel_hi:[1,0]
	v_mov_b32_dpp v92, v125 row_shr:1 row_mask:0xf bank_mask:0xf
	v_mov_b32_e32 v97, v125
	v_accvgpr_read_b32 v71, a15
	v_pk_add_f32 v[60:61], v[60:61], v[62:63]
	v_pk_mul_f32 v[62:63], v[96:97], v[92:93]
	v_accvgpr_read_b32 v70, a14
	v_mov_b32_dpp v59, v124 row_shl:1 row_mask:0xf bank_mask:0xf
	v_pk_fma_f32 v[62:63], v[124:125], v[16:17], v[62:63] op_sel_hi:[0,1,1]
	v_pk_mov_b32 v[68:69], v[124:125], v[70:71] op_sel:[1,0]
	v_mov_b32_e32 v94, v57
	v_pk_fma_f32 v[62:63], v[68:69], v[58:59], v[62:63]
	s_mov_b64 s[0:1], 0x820000
	v_pk_add_f32 v[60:61], v[60:61], v[62:63]
	v_mov_b32_dpp v94, v123 row_shr:1 row_mask:0xf bank_mask:0xf
	v_mov_b32_e32 v99, v123
	v_accvgpr_write_b32 a31, v17
	v_lshl_add_u64 v[62:63], v[54:55], 0, s[0:1]
	v_mov_b32_e32 v128, v60
	v_mov_b32_e32 v129, v61
	v_pk_mul_f32 v[60:61], v[98:99], v[94:95]
	v_mov_b32_e32 v102, v51
	v_accvgpr_write_b32 a30, v16
	v_mov_b32_dpp v57, v122 row_shl:1 row_mask:0xf bank_mask:0xf
	v_pk_fma_f32 v[60:61], v[122:123], v[28:29], v[60:61] op_sel_hi:[0,1,1]
	v_mov_b32_e32 v62, v123
	v_mov_b32_e32 v63, v67
	v_mov_b32_dpp v102, v121 row_shr:1 row_mask:0xf bank_mask:0xf
	v_mov_b32_e32 v105, v121
	v_accvgpr_read_b32 v16, a28
	v_pk_fma_f32 v[60:61], v[62:63], v[56:57], v[60:61]
	v_pk_mul_f32 v[62:63], v[104:105], v[102:103]
	v_accvgpr_read_b32 v17, a29
	v_mov_b32_dpp v51, v120 row_shl:1 row_mask:0xf bank_mask:0xf
	v_pk_fma_f32 v[62:63], v[120:121], v[16:17], v[62:63] op_sel_hi:[0,1,1]
	v_mov_b32_e32 v68, v121
	v_mov_b32_e32 v69, v15
	v_mov_b32_e32 v108, v49
	v_pk_fma_f32 v[62:63], v[68:69], v[50:51], v[62:63]
	v_pk_add_f32 v[60:61], v[60:61], 0 op_sel_hi:[1,0]
	v_mov_b32_dpp v108, v91 row_shr:1 row_mask:0xf bank_mask:0xf
	v_mov_b32_e32 v111, v91
	v_pk_add_f32 v[60:61], v[60:61], v[62:63]
	v_pk_mul_f32 v[62:63], v[110:111], v[108:109]
	v_mov_b32_dpp v49, v90 row_shl:1 row_mask:0xf bank_mask:0xf
	v_pk_fma_f32 v[62:63], v[90:91], v[30:31], v[62:63] op_sel_hi:[0,1,1]
	v_mov_b32_e32 v68, v91
	v_mov_b32_e32 v69, v71
	v_pk_fma_f32 v[62:63], v[68:69], v[48:49], v[62:63]
	s_mov_b64 s[0:1], 0x830000
	v_mov_b32_e32 v0, v22
	v_pk_add_f32 v[60:61], v[60:61], v[62:63]
	v_lshl_add_u64 v[136:137], v[134:135], 0, s[0:1]
	s_add_u32 s0, s10, 0x1c00000
	v_accvgpr_read_b32 v22, a50
	v_accvgpr_read_b32 v1, a72
	s_addc_u32 s1, s11, 0
	v_accvgpr_read_b32 v23, a51
	s_nop 1
	s_mov_b64 vcc, s[28:29]
	s_nop 0
	v_cndmask_b32_dpp v130, v60, v128, vcc quad_perm:[1,0,3,2] row_mask:0xf bank_mask:0xf
	v_cndmask_b32_dpp v131, v61, v129, vcc quad_perm:[1,0,3,2] row_mask:0xf bank_mask:0xf
	s_mov_b64 vcc, s[30:31]
	s_nop 0
	v_cndmask_b32_dpp v132, v128, v60, vcc quad_perm:[1,0,3,2] row_mask:0xf bank_mask:0xf
	v_cndmask_b32_dpp v133, v129, v61, vcc quad_perm:[1,0,3,2] row_mask:0xf bank_mask:0xf
	global_store_dwordx4 v[136:137], v[130:133], off sc0 sc1 nt
	s_nop 1
	v_readfirstlane_b32 s2, v1
	v_lshl_add_u64 v[60:61], s[0:1], 0, v[22:23]
	v_accvgpr_read_b32 v1, a12
	v_accvgpr_read_b32 v22, a52
	s_waitcnt vmcnt(18)
	s_mov_b32 m0, s2
	v_readfirstlane_b32 s2, v1
	v_accvgpr_read_b32 v23, a53
	v_accvgpr_read_b32 v1, a13
	s_waitcnt lgkmcnt(0)
	s_barrier
	global_load_lds_dwordx4 v[60:61], off nt
	v_lshl_add_u64 v[60:61], s[0:1], 0, v[22:23]
	s_mov_b32 m0, s2
	v_readfirstlane_b32 s2, v1
	v_accvgpr_read_b32 v1, a16
	global_load_lds_dwordx4 v[60:61], off nt
	v_lshl_add_u64 v[60:61], s[0:1], 0, v[114:115]
	s_mov_b32 m0, s2
	v_readfirstlane_b32 s2, v1
	global_load_lds_dwordx4 v[60:61], off nt
	v_lshl_add_u64 v[60:61], s[0:1], 0, v[116:117]
	s_mov_b32 m0, s2
	v_accvgpr_write_b32 a22, v30
	v_accvgpr_write_b32 a44, v70
	global_load_lds_dwordx4 v[60:61], off nt
	v_accvgpr_write_b32 a2, v106
	v_accvgpr_write_b32 a34, v74
	v_accvgpr_write_b32 a23, v31
	v_accvgpr_write_b32 a45, v71
	v_add_u32_e32 v2, 0x7010, v5
	v_mov_b32_e32 v31, v5
	v_add_u32_e32 v5, 0x7000, v4
	ds_read_b64 v[60:61], v2
	ds_read_b64 v[62:63], v2 offset:288
	ds_read_b64 v[68:69], v2 offset:576
	ds_read_b64 v[70:71], v2 offset:1728
	ds_read_b64 v[72:73], v2 offset:2016
	ds_read_b64 v[82:83], v2 offset:2304
	ds_read_b64 v[80:81], v2 offset:3456
	ds_read_b64 v[84:85], v2 offset:3744
	ds_read_b64 v[116:117], v2 offset:4032
	ds_read_b64 v[114:115], v2 offset:5184
	ds_read_b64 v[112:113], v2 offset:5472
	ds_read_b64 v[90:91], v2 offset:5760
	ds_read_b32 v43, v5
	ds_read_b32 v19, v5 offset:288
	ds_read_b32 v39, v5 offset:576
	ds_read_b32 v25, v5 offset:1728
	ds_read_b32 v7, v5 offset:2016
	ds_read_b32 v21, v5 offset:2304
	ds_read_b32 v11, v5 offset:3456
	ds_read_b32 v35, v5 offset:3744
	ds_read_b32 v59, v5 offset:4032
	ds_read_b32 v57, v5 offset:5184
	ds_read_b32 v51, v5 offset:5472
	ds_read_b32 v49, v5 offset:5760
	s_waitcnt lgkmcnt(0)
	v_accvgpr_write_b32 a3, v107
	v_mov_b32_e32 v46, v43
	v_accvgpr_write_b32 a35, v75
	v_accvgpr_read_b32 v74, a40
	v_mov_b32_dpp v46, v61 row_shr:1 row_mask:0xf bank_mask:0xf
	v_mov_b32_e32 v75, v61
	v_accvgpr_read_b32 v107, a39
	v_accvgpr_write_b32 a10, v100
	v_pk_mul_f32 v[86:87], v[74:75], v[46:47]
	v_accvgpr_read_b32 v106, a38
	v_mov_b32_e32 v26, v19
	v_accvgpr_write_b32 a11, v101
	v_mov_b32_dpp v43, v60 row_shl:1 row_mask:0xf bank_mask:0xf
	v_mov_b32_e32 v32, v74
	v_pk_fma_f32 v[86:87], v[60:61], v[8:9], v[86:87] op_sel_hi:[0,1,1]
	v_pk_mov_b32 v[60:61], v[60:61], v[106:107] op_sel:[1,0]
	v_mov_b32_dpp v26, v63 row_shr:1 row_mask:0xf bank_mask:0xf
	v_accvgpr_read_b32 v74, a24
	v_mov_b32_e32 v75, v63
	v_accvgpr_read_b32 v101, a35
	v_pk_fma_f32 v[60:61], v[60:61], v[42:43], v[86:87]
	v_pk_mul_f32 v[86:87], v[74:75], v[26:27]
	v_accvgpr_read_b32 v100, a34
	v_accvgpr_write_b32 a14, v66
	v_mov_b32_dpp v19, v62 row_shl:1 row_mask:0xf bank_mask:0xf
	v_pk_fma_f32 v[86:87], v[62:63], v[126:127], v[86:87] op_sel_hi:[0,1,1]
	v_pk_mov_b32 v[62:63], v[62:63], v[100:101] op_sel:[1,0]
	v_mov_b32_e32 v44, v39
	v_accvgpr_write_b32 a42, v64
	v_accvgpr_write_b32 a15, v67
	v_mov_b32_e32 v66, v4
	v_pk_fma_f32 v[62:63], v[62:63], v[18:19], v[86:87]
	v_pk_add_f32 v[60:61], v[60:61], 0 op_sel_hi:[1,0]
	v_mov_b32_dpp v44, v69 row_shr:1 row_mask:0xf bank_mask:0xf
	v_accvgpr_read_b32 v64, a48
	v_mov_b32_e32 v65, v69
	v_accvgpr_read_b32 v4, a46
	v_pk_add_f32 v[60:61], v[60:61], v[62:63]
	v_pk_mul_f32 v[62:63], v[64:65], v[44:45]
	v_accvgpr_read_b32 v5, a47
	v_mov_b32_dpp v39, v68 row_shl:1 row_mask:0xf bank_mask:0xf
	v_pk_fma_f32 v[62:63], v[68:69], v[88:89], v[62:63] op_sel_hi:[0,1,1]
	v_pk_mov_b32 v[68:69], v[68:69], v[4:5] op_sel:[1,0]
	v_mov_b32_e32 v36, v25
	v_pk_fma_f32 v[62:63], v[68:69], v[38:39], v[62:63]
	s_mov_b64 s[0:1], 0xc00000
	v_pk_add_f32 v[60:61], v[60:61], v[62:63]
	v_mov_b32_dpp v36, v71 row_shr:1 row_mask:0xf bank_mask:0xf
	v_accvgpr_read_b32 v22, a42
	v_mov_b32_e32 v23, v71
	v_accvgpr_mov_b32 a26, a20
	v_accvgpr_write_b32 a20, v28
	v_lshl_add_u64 v[62:63], v[54:55], 0, s[0:1]
	v_mov_b32_e32 v128, v60
	v_mov_b32_e32 v129, v61
	v_pk_mul_f32 v[60:61], v[22:23], v[36:37]
	v_mov_b32_e32 v12, v7
	v_accvgpr_write_b32 a21, v29
	v_mov_b32_dpp v25, v70 row_shl:1 row_mask:0xf bank_mask:0xf
	v_pk_fma_f32 v[60:61], v[70:71], v[118:119], v[60:61] op_sel_hi:[0,1,1]
	v_mov_b32_e32 v62, v71
	v_mov_b32_e32 v63, v107
	v_mov_b32_dpp v12, v73 row_shr:1 row_mask:0xf bank_mask:0xf
	v_accvgpr_read_b32 v28, a26
	v_mov_b32_e32 v29, v73
	v_accvgpr_read_b32 v121, a3
	v_pk_fma_f32 v[60:61], v[62:63], v[24:25], v[60:61]
	v_pk_mul_f32 v[62:63], v[28:29], v[12:13]
	v_accvgpr_read_b32 v120, a2
	v_mov_b32_dpp v7, v72 row_shl:1 row_mask:0xf bank_mask:0xf
	v_pk_fma_f32 v[62:63], v[72:73], v[120:121], v[62:63] op_sel_hi:[0,1,1]
	v_mov_b32_e32 v68, v73
	v_mov_b32_e32 v69, v101
	v_mov_b32_e32 v78, v21
	v_pk_fma_f32 v[62:63], v[68:69], v[6:7], v[62:63]
	v_pk_add_f32 v[60:61], v[60:61], 0 op_sel_hi:[1,0]
	v_mov_b32_dpp v78, v83 row_shr:1 row_mask:0xf bank_mask:0xf
	v_mov_b32_e32 v53, v83
	v_accvgpr_read_b32 v125, a19
	v_pk_add_f32 v[60:61], v[60:61], v[62:63]
	v_pk_mul_f32 v[62:63], v[52:53], v[78:79]
	v_accvgpr_read_b32 v124, a18
	v_mov_b32_dpp v21, v82 row_shl:1 row_mask:0xf bank_mask:0xf
	v_pk_fma_f32 v[62:63], v[82:83], v[124:125], v[62:63] op_sel_hi:[0,1,1]
	v_mov_b32_e32 v68, v83
	v_mov_b32_e32 v69, v5
	v_pk_fma_f32 v[62:63], v[68:69], v[20:21], v[62:63]
	v_mov_b32_e32 v76, v11
	v_pk_add_f32 v[60:61], v[60:61], v[62:63]
	s_mov_b64 s[0:1], 0xc10000
	v_mov_b32_dpp v76, v81 row_shr:1 row_mask:0xf bank_mask:0xf
	v_mov_b32_e32 v41, v81
	v_accvgpr_read_b32 v123, a37
	v_accvgpr_read_b32 v4, a14
	v_lshl_add_u64 v[136:137], v[134:135], 0, s[0:1]
	s_nop 1
	s_mov_b64 vcc, s[28:29]
	s_nop 0
	v_cndmask_b32_dpp v130, v60, v128, vcc quad_perm:[1,0,3,2] row_mask:0xf bank_mask:0xf
	v_cndmask_b32_dpp v131, v61, v129, vcc quad_perm:[1,0,3,2] row_mask:0xf bank_mask:0xf
	s_mov_b64 vcc, s[30:31]
	s_nop 0
	v_cndmask_b32_dpp v132, v128, v60, vcc quad_perm:[1,0,3,2] row_mask:0xf bank_mask:0xf
	v_cndmask_b32_dpp v133, v129, v61, vcc quad_perm:[1,0,3,2] row_mask:0xf bank_mask:0xf
	global_store_dwordx4 v[136:137], v[130:133], off sc0 sc1 nt
	s_nop 1
	v_pk_mul_f32 v[60:61], v[40:41], v[76:77]
	v_accvgpr_read_b32 v122, a36
	v_accvgpr_read_b32 v5, a15
	v_mov_b32_e32 v2, v35
	v_accvgpr_mov_b32 a32, a24
	v_accvgpr_write_b32 a24, v22
	v_mov_b64_e32 v[22:23], v[118:119]
	v_mov_b32_dpp v11, v80 row_shl:1 row_mask:0xf bank_mask:0xf
	v_pk_fma_f32 v[60:61], v[80:81], v[122:123], v[60:61] op_sel_hi:[0,1,1]
	v_pk_mov_b32 v[62:63], v[80:81], v[4:5] op_sel:[1,0]
	v_mov_b32_dpp v2, v85 row_shr:1 row_mask:0xf bank_mask:0xf
	v_mov_b32_e32 v106, v0
	v_mov_b32_e32 v107, v85
	v_accvgpr_read_b32 v119, a11
	v_pk_fma_f32 v[60:61], v[62:63], v[10:11], v[60:61]
	v_pk_mul_f32 v[62:63], v[106:107], v[2:3]
	v_accvgpr_read_b32 v118, a10
	v_mov_b64_e32 v[100:101], v[14:15]
	v_mov_b32_dpp v35, v84 row_shl:1 row_mask:0xf bank_mask:0xf
	v_pk_fma_f32 v[62:63], v[84:85], v[118:119], v[62:63] op_sel_hi:[0,1,1]
	v_pk_mov_b32 v[68:69], v[84:85], v[100:101] op_sel:[1,0]
	v_mov_b32_e32 v92, v59
	v_accvgpr_write_b32 a26, v52
	v_mov_b32_e32 v74, v40
	v_pk_fma_f32 v[62:63], v[68:69], v[34:35], v[62:63]
	v_pk_add_f32 v[60:61], v[60:61], 0 op_sel_hi:[1,0]
	v_mov_b32_dpp v92, v117 row_shr:1 row_mask:0xf bank_mask:0xf
	v_mov_b32_e32 v97, v117
	v_accvgpr_read_b32 v41, a31
	v_accvgpr_read_b32 v53, a45
	v_pk_add_f32 v[60:61], v[60:61], v[62:63]
	v_pk_mul_f32 v[62:63], v[96:97], v[92:93]
	v_accvgpr_read_b32 v40, a30
	v_accvgpr_read_b32 v52, a44
	v_mov_b32_dpp v59, v116 row_shl:1 row_mask:0xf bank_mask:0xf
	v_pk_fma_f32 v[62:63], v[116:117], v[40:41], v[62:63] op_sel_hi:[0,1,1]
	v_pk_mov_b32 v[68:69], v[116:117], v[52:53] op_sel:[1,0]
	v_mov_b32_e32 v94, v57
	v_pk_fma_f32 v[62:63], v[68:69], v[58:59], v[62:63]
	s_mov_b64 s[0:1], 0xc20000
	v_pk_add_f32 v[60:61], v[60:61], v[62:63]
	v_mov_b32_dpp v94, v115 row_shr:1 row_mask:0xf bank_mask:0xf
	v_mov_b32_e32 v99, v115
	v_accvgpr_read_b32 v14, a20
	v_lshl_add_u64 v[62:63], v[54:55], 0, s[0:1]
	v_mov_b32_e32 v128, v60
	v_mov_b32_e32 v129, v61
	v_pk_mul_f32 v[60:61], v[98:99], v[94:95]
	v_accvgpr_read_b32 v15, a21
	v_mov_b32_e32 v102, v51
	v_mov_b32_dpp v57, v114 row_shl:1 row_mask:0xf bank_mask:0xf
	v_pk_fma_f32 v[60:61], v[114:115], v[14:15], v[60:61] op_sel_hi:[0,1,1]
	v_mov_b32_e32 v62, v115
	v_mov_b32_e32 v63, v5
	v_mov_b32_dpp v102, v113 row_shr:1 row_mask:0xf bank_mask:0xf
	v_mov_b32_e32 v105, v113
	v_pk_fma_f32 v[60:61], v[62:63], v[56:57], v[60:61]
	v_pk_mul_f32 v[62:63], v[104:105], v[102:103]
	v_accvgpr_write_b32 a8, v8
	v_mov_b32_dpp v51, v112 row_shl:1 row_mask:0xf bank_mask:0xf
	v_pk_fma_f32 v[62:63], v[112:113], v[16:17], v[62:63] op_sel_hi:[0,1,1]
	v_mov_b32_e32 v68, v113
	v_mov_b32_e32 v69, v101
	v_mov_b32_e32 v108, v49
	v_accvgpr_write_b32 a9, v9
	v_pk_fma_f32 v[62:63], v[68:69], v[50:51], v[62:63]
	v_pk_add_f32 v[60:61], v[60:61], 0 op_sel_hi:[1,0]
	v_mov_b32_dpp v108, v91 row_shr:1 row_mask:0xf bank_mask:0xf
	v_mov_b32_e32 v111, v91
	v_accvgpr_read_b32 v8, a22
	v_pk_add_f32 v[60:61], v[60:61], v[62:63]
	v_pk_mul_f32 v[62:63], v[110:111], v[108:109]
	v_accvgpr_read_b32 v9, a23
	v_mov_b32_dpp v49, v90 row_shl:1 row_mask:0xf bank_mask:0xf
	v_pk_fma_f32 v[62:63], v[90:91], v[8:9], v[62:63] op_sel_hi:[0,1,1]
	v_mov_b32_e32 v68, v91
	v_mov_b32_e32 v69, v53
	v_pk_fma_f32 v[62:63], v[68:69], v[48:49], v[62:63]
	s_mov_b64 s[0:1], 0xc30000
	v_pk_add_f32 v[60:61], v[60:61], v[62:63]
	v_lshl_add_u64 v[136:137], v[134:135], 0, s[0:1]
	s_nop 1
	s_mov_b64 vcc, s[28:29]
	s_nop 0
	v_cndmask_b32_dpp v130, v60, v128, vcc quad_perm:[1,0,3,2] row_mask:0xf bank_mask:0xf
	v_cndmask_b32_dpp v131, v61, v129, vcc quad_perm:[1,0,3,2] row_mask:0xf bank_mask:0xf
	s_mov_b64 vcc, s[30:31]
	s_nop 0
	v_cndmask_b32_dpp v132, v128, v60, vcc quad_perm:[1,0,3,2] row_mask:0xf bank_mask:0xf
	v_cndmask_b32_dpp v133, v129, v61, vcc quad_perm:[1,0,3,2] row_mask:0xf bank_mask:0xf
	global_store_dwordx4 v[136:137], v[130:133], off sc0 sc1 nt
	s_nop 1
	s_waitcnt vmcnt(20)
	v_accvgpr_write_b32 a16, v88
	v_accvgpr_write_b32 a10, v100
	s_waitcnt lgkmcnt(0)
	s_barrier
	v_add_u32_e32 v2, 0xe010, v31
	v_add_u32_e32 v5, 0xe000, v66
	ds_read_b64 v[60:61], v2
	ds_read_b64 v[62:63], v2 offset:288
	ds_read_b64 v[68:69], v2 offset:576
	ds_read_b64 v[70:71], v2 offset:1728
	ds_read_b64 v[72:73], v2 offset:2016
	ds_read_b64 v[82:83], v2 offset:2304
	ds_read_b64 v[80:81], v2 offset:3456
	ds_read_b64 v[84:85], v2 offset:3744
	ds_read_b64 v[116:117], v2 offset:4032
	ds_read_b64 v[114:115], v2 offset:5184
	ds_read_b64 v[112:113], v2 offset:5472
	ds_read_b64 v[90:91], v2 offset:5760
	ds_read_b32 v43, v5
	ds_read_b32 v19, v5 offset:288
	ds_read_b32 v39, v5 offset:576
	ds_read_b32 v25, v5 offset:1728
	ds_read_b32 v7, v5 offset:2016
	ds_read_b32 v21, v5 offset:2304
	ds_read_b32 v11, v5 offset:3456
	ds_read_b32 v35, v5 offset:3744
	ds_read_b32 v59, v5 offset:4032
	ds_read_b32 v57, v5 offset:5184
	ds_read_b32 v51, v5 offset:5472
	ds_read_b32 v49, v5 offset:5760
	s_waitcnt lgkmcnt(0)
	v_accvgpr_write_b32 a17, v89
	v_mov_b32_e32 v46, v43
	v_accvgpr_write_b32 a11, v101
	v_mov_b32_e32 v33, v61
	v_mov_b32_dpp v46, v61 row_shr:1 row_mask:0xf bank_mask:0xf
	v_accvgpr_read_b32 v89, a9
	v_accvgpr_read_b32 v101, a39
	v_pk_mul_f32 v[86:87], v[32:33], v[46:47]
	v_accvgpr_read_b32 v88, a8
	v_accvgpr_read_b32 v100, a38
	v_mov_b32_e32 v26, v19
	v_accvgpr_write_b32 a19, v17
	v_mov_b32_dpp v43, v60 row_shl:1 row_mask:0xf bank_mask:0xf
	v_pk_fma_f32 v[86:87], v[60:61], v[88:89], v[86:87] op_sel_hi:[0,1,1]
	v_pk_mov_b32 v[60:61], v[60:61], v[100:101] op_sel:[1,0]
	v_mov_b32_dpp v26, v63 row_shr:1 row_mask:0xf bank_mask:0xf
	v_accvgpr_read_b32 v0, a32
	v_mov_b32_e32 v1, v63
	v_accvgpr_read_b32 v4, a34
	v_accvgpr_write_b32 a18, v16
	v_pk_fma_f32 v[60:61], v[60:61], v[42:43], v[86:87]
	v_pk_mul_f32 v[86:87], v[0:1], v[26:27]
	v_mov_b64_e32 v[16:17], v[126:127]
	v_accvgpr_read_b32 v5, a35
	v_mov_b32_dpp v19, v62 row_shl:1 row_mask:0xf bank_mask:0xf
	v_pk_fma_f32 v[86:87], v[62:63], v[16:17], v[86:87] op_sel_hi:[0,1,1]
	v_pk_mov_b32 v[62:63], v[62:63], v[4:5] op_sel:[1,0]
	v_mov_b32_e32 v44, v39
	v_accvgpr_read_b32 v30, a48
	v_mov_b32_e32 v64, v28
	v_accvgpr_write_b32 a7, v66
	v_pk_fma_f32 v[62:63], v[62:63], v[18:19], v[86:87]
	v_pk_add_f32 v[60:61], v[60:61], 0 op_sel_hi:[1,0]
	v_mov_b32_dpp v44, v69 row_shr:1 row_mask:0xf bank_mask:0xf
	v_mov_b32_e32 v31, v69
	v_accvgpr_read_b32 v29, a17
	v_accvgpr_read_b32 v67, a47
	v_pk_add_f32 v[60:61], v[60:61], v[62:63]
	v_pk_mul_f32 v[62:63], v[30:31], v[44:45]
	v_accvgpr_read_b32 v28, a16
	v_accvgpr_read_b32 v66, a46
	v_mov_b32_dpp v39, v68 row_shl:1 row_mask:0xf bank_mask:0xf
	v_pk_fma_f32 v[62:63], v[68:69], v[28:29], v[62:63] op_sel_hi:[0,1,1]
	v_pk_mov_b32 v[68:69], v[68:69], v[66:67] op_sel:[1,0]
	v_mov_b32_e32 v36, v25
	v_pk_fma_f32 v[62:63], v[68:69], v[38:39], v[62:63]
	s_mov_b64 s[0:1], 0x1000000
	v_pk_add_f32 v[60:61], v[60:61], v[62:63]
	v_mov_b32_dpp v36, v71 row_shr:1 row_mask:0xf bank_mask:0xf
	v_accvgpr_read_b32 v126, a24
	v_mov_b32_e32 v127, v71
	v_lshl_add_u64 v[62:63], v[54:55], 0, s[0:1]
	v_mov_b32_e32 v128, v60
	v_mov_b32_e32 v129, v61
	v_pk_mul_f32 v[60:61], v[126:127], v[36:37]
	v_mov_b32_e32 v12, v7
	v_mov_b32_dpp v25, v70 row_shl:1 row_mask:0xf bank_mask:0xf
	v_pk_fma_f32 v[60:61], v[70:71], v[22:23], v[60:61] op_sel_hi:[0,1,1]
	v_mov_b32_e32 v62, v71
	v_mov_b32_e32 v63, v101
	v_mov_b32_dpp v12, v73 row_shr:1 row_mask:0xf bank_mask:0xf
	v_mov_b32_e32 v52, v64
	v_mov_b32_e32 v53, v73
	v_pk_fma_f32 v[60:61], v[62:63], v[24:25], v[60:61]
	v_pk_mul_f32 v[62:63], v[52:53], v[12:13]
	v_mov_b32_dpp v7, v72 row_shl:1 row_mask:0xf bank_mask:0xf
	v_pk_fma_f32 v[62:63], v[72:73], v[120:121], v[62:63] op_sel_hi:[0,1,1]
	v_mov_b32_e32 v68, v73
	v_mov_b32_e32 v69, v5
	v_mov_b32_e32 v78, v21
	v_pk_fma_f32 v[62:63], v[68:69], v[6:7], v[62:63]
	v_pk_add_f32 v[60:61], v[60:61], 0 op_sel_hi:[1,0]
	v_mov_b32_dpp v78, v83 row_shr:1 row_mask:0xf bank_mask:0xf
	v_accvgpr_read_b32 v4, a26
	v_mov_b32_e32 v5, v83
	v_pk_add_f32 v[60:61], v[60:61], v[62:63]
	v_pk_mul_f32 v[62:63], v[4:5], v[78:79]
	v_mov_b32_dpp v21, v82 row_shl:1 row_mask:0xf bank_mask:0xf
	v_pk_fma_f32 v[62:63], v[82:83], v[124:125], v[62:63] op_sel_hi:[0,1,1]
	v_mov_b32_e32 v68, v83
	v_mov_b32_e32 v69, v67
	v_accvgpr_write_b32 a8, v120
	v_pk_fma_f32 v[62:63], v[68:69], v[20:21], v[62:63]
	v_mov_b32_e32 v76, v11
	v_accvgpr_write_b32 a9, v121
	v_pk_add_f32 v[60:61], v[60:61], v[62:63]
	s_mov_b64 s[0:1], 0x1010000
	v_mov_b32_dpp v76, v81 row_shr:1 row_mask:0xf bank_mask:0xf
	v_mov_b32_e32 v120, v74
	v_mov_b32_e32 v121, v81
	v_accvgpr_read_b32 v101, a15
	v_accvgpr_mov_b32 a12, a38
	v_lshl_add_u64 v[136:137], v[134:135], 0, s[0:1]
	s_nop 1
	s_mov_b64 vcc, s[28:29]
	s_nop 0
	v_cndmask_b32_dpp v130, v60, v128, vcc quad_perm:[1,0,3,2] row_mask:0xf bank_mask:0xf
	v_cndmask_b32_dpp v131, v61, v129, vcc quad_perm:[1,0,3,2] row_mask:0xf bank_mask:0xf
	s_mov_b64 vcc, s[30:31]
	s_nop 0
	v_cndmask_b32_dpp v132, v128, v60, vcc quad_perm:[1,0,3,2] row_mask:0xf bank_mask:0xf
	v_cndmask_b32_dpp v133, v129, v61, vcc quad_perm:[1,0,3,2] row_mask:0xf bank_mask:0xf
	global_store_dwordx4 v[136:137], v[130:133], off sc0 sc1 nt
	s_nop 1
	v_pk_mul_f32 v[60:61], v[120:121], v[76:77]
	v_accvgpr_read_b32 v100, a14
	v_mov_b32_e32 v2, v35
	v_accvgpr_mov_b32 a13, a39
	v_accvgpr_write_b32 a20, v22
	v_mov_b32_dpp v11, v80 row_shl:1 row_mask:0xf bank_mask:0xf
	v_pk_fma_f32 v[60:61], v[80:81], v[122:123], v[60:61] op_sel_hi:[0,1,1]
	v_pk_mov_b32 v[62:63], v[80:81], v[100:101] op_sel:[1,0]
	v_mov_b32_dpp v2, v85 row_shr:1 row_mask:0xf bank_mask:0xf
	v_mov_b32_e32 v107, v85
	v_accvgpr_read_b32 v123, a11
	v_accvgpr_write_b32 a21, v23
	v_accvgpr_read_b32 v23, a13
	v_pk_fma_f32 v[60:61], v[62:63], v[10:11], v[60:61]
	v_pk_mul_f32 v[62:63], v[106:107], v[2:3]
	v_accvgpr_read_b32 v122, a10
	v_accvgpr_read_b32 v22, a12
	v_mov_b32_dpp v35, v84 row_shl:1 row_mask:0xf bank_mask:0xf
	v_pk_fma_f32 v[62:63], v[84:85], v[118:119], v[62:63] op_sel_hi:[0,1,1]
	v_accvgpr_write_b32 a12, v118
	v_pk_mov_b32 v[68:69], v[84:85], v[122:123] op_sel:[1,0]
	v_mov_b32_e32 v92, v59
	v_accvgpr_write_b32 a13, v119
	v_pk_fma_f32 v[62:63], v[68:69], v[34:35], v[62:63]
	v_pk_add_f32 v[60:61], v[60:61], 0 op_sel_hi:[1,0]
	v_mov_b32_dpp v92, v117 row_shr:1 row_mask:0xf bank_mask:0xf
	v_mov_b32_e32 v97, v117
	v_mov_b64_e32 v[118:119], v[40:41]
	v_accvgpr_read_b32 v40, a44
	v_pk_add_f32 v[60:61], v[60:61], v[62:63]
	v_pk_mul_f32 v[62:63], v[96:97], v[92:93]
	v_accvgpr_read_b32 v41, a45
	v_mov_b32_dpp v59, v116 row_shl:1 row_mask:0xf bank_mask:0xf
	v_pk_fma_f32 v[62:63], v[116:117], v[118:119], v[62:63] op_sel_hi:[0,1,1]
	v_pk_mov_b32 v[68:69], v[116:117], v[40:41] op_sel:[1,0]
	v_mov_b32_e32 v94, v57
	v_pk_fma_f32 v[62:63], v[68:69], v[58:59], v[62:63]
	s_mov_b64 s[0:1], 0x1020000
	v_pk_add_f32 v[60:61], v[60:61], v[62:63]
	v_mov_b32_dpp v94, v115 row_shr:1 row_mask:0xf bank_mask:0xf
	v_mov_b32_e32 v99, v115
	v_lshl_add_u64 v[62:63], v[54:55], 0, s[0:1]
	v_mov_b32_e32 v128, v60
	v_mov_b32_e32 v129, v61
	v_pk_mul_f32 v[60:61], v[98:99], v[94:95]
	v_mov_b32_e32 v102, v51
	v_accvgpr_write_b32 a30, v4
	v_mov_b32_dpp v57, v114 row_shl:1 row_mask:0xf bank_mask:0xf
	v_pk_fma_f32 v[60:61], v[114:115], v[14:15], v[60:61] op_sel_hi:[0,1,1]
	v_mov_b32_e32 v62, v115
	v_mov_b32_e32 v63, v101
	v_mov_b32_dpp v102, v113 row_shr:1 row_mask:0xf bank_mask:0xf
	v_mov_b32_e32 v105, v113
	v_accvgpr_read_b32 v4, a18
	v_pk_fma_f32 v[60:61], v[62:63], v[56:57], v[60:61]
	v_pk_mul_f32 v[62:63], v[104:105], v[102:103]
	v_accvgpr_read_b32 v5, a19
	v_mov_b32_dpp v51, v112 row_shl:1 row_mask:0xf bank_mask:0xf
	v_pk_fma_f32 v[62:63], v[112:113], v[4:5], v[62:63] op_sel_hi:[0,1,1]
	v_mov_b32_e32 v68, v113
	v_mov_b32_e32 v69, v123
	v_mov_b32_e32 v108, v49
	v_pk_fma_f32 v[62:63], v[68:69], v[50:51], v[62:63]
	v_pk_add_f32 v[60:61], v[60:61], 0 op_sel_hi:[1,0]
	v_mov_b32_dpp v108, v91 row_shr:1 row_mask:0xf bank_mask:0xf
	v_mov_b32_e32 v111, v91
	v_pk_add_f32 v[60:61], v[60:61], v[62:63]
	v_pk_mul_f32 v[62:63], v[110:111], v[108:109]
	v_mov_b32_dpp v49, v90 row_shl:1 row_mask:0xf bank_mask:0xf
	v_pk_fma_f32 v[62:63], v[90:91], v[8:9], v[62:63] op_sel_hi:[0,1,1]
	v_mov_b32_e32 v68, v91
	v_mov_b32_e32 v69, v41
	v_pk_fma_f32 v[62:63], v[68:69], v[48:49], v[62:63]
	s_mov_b64 s[0:1], 0x1030000
	v_pk_add_f32 v[60:61], v[60:61], v[62:63]
	v_lshl_add_u64 v[136:137], v[134:135], 0, s[0:1]
	s_nop 1
	s_mov_b64 vcc, s[28:29]
	s_nop 0
	v_cndmask_b32_dpp v130, v60, v128, vcc quad_perm:[1,0,3,2] row_mask:0xf bank_mask:0xf
	v_cndmask_b32_dpp v131, v61, v129, vcc quad_perm:[1,0,3,2] row_mask:0xf bank_mask:0xf
	s_mov_b64 vcc, s[30:31]
	s_nop 0
	v_cndmask_b32_dpp v132, v128, v60, vcc quad_perm:[1,0,3,2] row_mask:0xf bank_mask:0xf
	v_cndmask_b32_dpp v133, v129, v61, vcc quad_perm:[1,0,3,2] row_mask:0xf bank_mask:0xf
	global_store_dwordx4 v[136:137], v[130:133], off sc0 sc1 nt
	s_nop 1
	s_waitcnt vmcnt(16)
	s_waitcnt lgkmcnt(0)
	s_barrier
	v_accvgpr_read_b32 v2, a0
	v_accvgpr_read_b32 v8, a4
	ds_read_b64 v[60:61], v8
	ds_read_b64 v[62:63], v8 offset:288
	ds_read_b64 v[68:69], v8 offset:576
	ds_read_b64 v[70:71], v8 offset:1728
	ds_read_b64 v[72:73], v8 offset:2016
	ds_read_b64 v[82:83], v8 offset:2304
	ds_read_b64 v[80:81], v8 offset:3456
	ds_read_b64 v[84:85], v8 offset:3744
	ds_read_b64 v[116:117], v8 offset:4032
	ds_read_b64 v[114:115], v8 offset:5184
	ds_read_b64 v[112:113], v8 offset:5472
	ds_read_b64 v[90:91], v8 offset:5760
	ds_read_b32 v43, v2
	ds_read_b32 v19, v2 offset:288
	ds_read_b32 v39, v2 offset:576
	ds_read_b32 v25, v2 offset:1728
	ds_read_b32 v7, v2 offset:2016
	ds_read_b32 v21, v2 offset:2304
	ds_read_b32 v11, v2 offset:3456
	ds_read_b32 v35, v2 offset:3744
	ds_read_b32 v59, v2 offset:4032
	ds_read_b32 v57, v2 offset:5184
	ds_read_b32 v51, v2 offset:5472
	ds_read_b32 v49, v2 offset:5760
	s_waitcnt lgkmcnt(0)
	v_mov_b32_e32 v64, v32
	v_mov_b32_e32 v46, v43
	v_mov_b32_e32 v65, v61
	v_mov_b64_e32 v[100:101], v[22:23]
	v_mov_b32_dpp v46, v61 row_shr:1 row_mask:0xf bank_mask:0xf
	v_pk_mul_f32 v[86:87], v[64:65], v[46:47]
	v_mov_b32_e32 v26, v19
	v_mov_b32_dpp v43, v60 row_shl:1 row_mask:0xf bank_mask:0xf
	v_pk_fma_f32 v[86:87], v[60:61], v[88:89], v[86:87] op_sel_hi:[0,1,1]
	v_pk_mov_b32 v[60:61], v[60:61], v[100:101] op_sel:[1,0]
	v_mov_b32_dpp v26, v63 row_shr:1 row_mask:0xf bank_mask:0xf
	v_mov_b32_e32 v1, v63
	v_accvgpr_read_b32 v67, a35
	v_pk_fma_f32 v[60:61], v[60:61], v[42:43], v[86:87]
	v_pk_mul_f32 v[86:87], v[0:1], v[26:27]
	v_accvgpr_read_b32 v66, a34
	v_accvgpr_write_b32 a10, v14
	v_mov_b32_dpp v19, v62 row_shl:1 row_mask:0xf bank_mask:0xf
	v_pk_fma_f32 v[86:87], v[62:63], v[16:17], v[86:87] op_sel_hi:[0,1,1]
	v_pk_mov_b32 v[62:63], v[62:63], v[66:67] op_sel:[1,0]
	v_mov_b32_e32 v44, v39
	v_accvgpr_write_b32 a11, v15
	v_pk_fma_f32 v[62:63], v[62:63], v[18:19], v[86:87]
	v_pk_add_f32 v[60:61], v[60:61], 0 op_sel_hi:[1,0]
	v_mov_b32_dpp v44, v69 row_shr:1 row_mask:0xf bank_mask:0xf
	v_mov_b32_e32 v31, v69
	v_accvgpr_read_b32 v14, a16
	v_accvgpr_read_b32 v28, a46
	v_pk_add_f32 v[60:61], v[60:61], v[62:63]
	v_pk_mul_f32 v[62:63], v[30:31], v[44:45]
	v_accvgpr_read_b32 v15, a17
	v_accvgpr_read_b32 v29, a47
	v_mov_b32_dpp v39, v68 row_shl:1 row_mask:0xf bank_mask:0xf
	v_pk_fma_f32 v[62:63], v[68:69], v[14:15], v[62:63] op_sel_hi:[0,1,1]
	v_pk_mov_b32 v[68:69], v[68:69], v[28:29] op_sel:[1,0]
	v_mov_b32_e32 v36, v25
	v_pk_fma_f32 v[62:63], v[68:69], v[38:39], v[62:63]
	s_mov_b64 s[0:1], 0x1400000
	v_pk_add_f32 v[60:61], v[60:61], v[62:63]
	v_mov_b32_dpp v36, v71 row_shr:1 row_mask:0xf bank_mask:0xf
	v_mov_b32_e32 v127, v71
	v_accvgpr_read_b32 v8, a20
	v_lshl_add_u64 v[62:63], v[54:55], 0, s[0:1]
	v_mov_b32_e32 v128, v60
	v_mov_b32_e32 v129, v61
	v_pk_mul_f32 v[60:61], v[126:127], v[36:37]
	v_accvgpr_read_b32 v9, a21
	v_accvgpr_write_b32 a25, v23
	v_mov_b32_e32 v12, v7
	v_mov_b32_dpp v25, v70 row_shl:1 row_mask:0xf bank_mask:0xf
	v_pk_fma_f32 v[60:61], v[70:71], v[8:9], v[60:61] op_sel_hi:[0,1,1]
	v_mov_b32_e32 v62, v71
	v_mov_b32_e32 v63, v101
	v_accvgpr_write_b32 a24, v22
	v_mov_b32_dpp v12, v73 row_shr:1 row_mask:0xf bank_mask:0xf
	v_mov_b32_e32 v74, v52
	v_mov_b32_e32 v75, v73
	v_accvgpr_read_b32 v23, a9
	v_accvgpr_write_b32 a26, v124
	v_accvgpr_mov_b32 a2, a22
	v_pk_fma_f32 v[60:61], v[62:63], v[24:25], v[60:61]
	v_pk_mul_f32 v[62:63], v[74:75], v[12:13]
	v_accvgpr_read_b32 v22, a8
	v_accvgpr_write_b32 a27, v125
	v_accvgpr_mov_b32 a3, a23
	v_accvgpr_write_b32 a22, v88
	v_mov_b32_dpp v7, v72 row_shl:1 row_mask:0xf bank_mask:0xf
	v_pk_fma_f32 v[62:63], v[72:73], v[22:23], v[62:63] op_sel_hi:[0,1,1]
	v_mov_b32_e32 v68, v73
	v_mov_b32_e32 v69, v67
	v_mov_b32_e32 v78, v21
	v_accvgpr_write_b32 a23, v89
	v_pk_fma_f32 v[62:63], v[68:69], v[6:7], v[62:63]
	v_pk_add_f32 v[60:61], v[60:61], 0 op_sel_hi:[1,0]
	v_mov_b32_dpp v78, v83 row_shr:1 row_mask:0xf bank_mask:0xf
	v_accvgpr_read_b32 v52, a30
	v_mov_b32_e32 v53, v83
	v_accvgpr_read_b32 v89, a27
	v_pk_add_f32 v[60:61], v[60:61], v[62:63]
	v_pk_mul_f32 v[62:63], v[52:53], v[78:79]
	v_accvgpr_read_b32 v88, a26
	v_mov_b32_dpp v21, v82 row_shl:1 row_mask:0xf bank_mask:0xf
	v_pk_fma_f32 v[62:63], v[82:83], v[88:89], v[62:63] op_sel_hi:[0,1,1]
	v_mov_b32_e32 v68, v83
	v_mov_b32_e32 v69, v29
	v_pk_fma_f32 v[62:63], v[68:69], v[20:21], v[62:63]
	v_mov_b32_e32 v76, v11
	v_accvgpr_read_b32 v125, a37
	v_pk_add_f32 v[60:61], v[60:61], v[62:63]
	s_mov_b64 s[0:1], 0x1410000
	v_mov_b32_dpp v76, v81 row_shr:1 row_mask:0xf bank_mask:0xf
	v_mov_b32_e32 v121, v81
	v_accvgpr_read_b32 v101, a15
	v_accvgpr_read_b32 v124, a36
	v_lshl_add_u64 v[136:137], v[134:135], 0, s[0:1]
	s_nop 1
	s_mov_b64 vcc, s[28:29]
	s_nop 0
	v_cndmask_b32_dpp v130, v60, v128, vcc quad_perm:[1,0,3,2] row_mask:0xf bank_mask:0xf
	v_cndmask_b32_dpp v131, v61, v129, vcc quad_perm:[1,0,3,2] row_mask:0xf bank_mask:0xf
	s_mov_b64 vcc, s[30:31]
	s_nop 0
	v_cndmask_b32_dpp v132, v128, v60, vcc quad_perm:[1,0,3,2] row_mask:0xf bank_mask:0xf
	v_cndmask_b32_dpp v133, v129, v61, vcc quad_perm:[1,0,3,2] row_mask:0xf bank_mask:0xf
	global_store_dwordx4 v[136:137], v[130:133], off sc0 sc1 nt
	s_nop 1
	v_pk_mul_f32 v[60:61], v[120:121], v[76:77]
	v_accvgpr_read_b32 v100, a14
	v_mov_b32_e32 v2, v35
	v_mov_b32_dpp v11, v80 row_shl:1 row_mask:0xf bank_mask:0xf
	v_pk_fma_f32 v[60:61], v[80:81], v[124:125], v[60:61] op_sel_hi:[0,1,1]
	v_pk_mov_b32 v[62:63], v[80:81], v[100:101] op_sel:[1,0]
	v_mov_b32_dpp v2, v85 row_shr:1 row_mask:0xf bank_mask:0xf
	v_mov_b32_e32 v107, v85
	v_accvgpr_read_b32 v29, a13
	v_pk_fma_f32 v[60:61], v[62:63], v[10:11], v[60:61]
	v_pk_mul_f32 v[62:63], v[106:107], v[2:3]
	v_accvgpr_read_b32 v28, a12
	v_mov_b32_dpp v35, v84 row_shl:1 row_mask:0xf bank_mask:0xf
	v_pk_fma_f32 v[62:63], v[84:85], v[28:29], v[62:63] op_sel_hi:[0,1,1]
	v_pk_mov_b32 v[68:69], v[84:85], v[122:123] op_sel:[1,0]
	v_mov_b32_e32 v92, v59
	v_pk_fma_f32 v[62:63], v[68:69], v[34:35], v[62:63]
	v_pk_add_f32 v[60:61], v[60:61], 0 op_sel_hi:[1,0]
	v_mov_b32_dpp v92, v117 row_shr:1 row_mask:0xf bank_mask:0xf
	v_mov_b32_e32 v97, v117
	v_pk_add_f32 v[60:61], v[60:61], v[62:63]
	v_pk_mul_f32 v[62:63], v[96:97], v[92:93]
	v_accvgpr_write_b32 a8, v118
	v_pk_fma_f32 v[62:63], v[116:117], v[118:119], v[62:63] op_sel_hi:[0,1,1]
	v_accvgpr_write_b32 a9, v119
	v_accvgpr_read_b32 v119, a45
	v_accvgpr_read_b32 v118, a44
	v_mov_b32_dpp v59, v116 row_shl:1 row_mask:0xf bank_mask:0xf
	v_pk_mov_b32 v[68:69], v[116:117], v[118:119] op_sel:[1,0]
	v_mov_b32_e32 v94, v57
	v_pk_fma_f32 v[62:63], v[68:69], v[58:59], v[62:63]
	s_mov_b64 s[0:1], 0x1420000
	v_pk_add_f32 v[60:61], v[60:61], v[62:63]
	v_mov_b32_dpp v94, v115 row_shr:1 row_mask:0xf bank_mask:0xf
	v_mov_b32_e32 v99, v115
	v_accvgpr_read_b32 v41, a11
	v_lshl_add_u64 v[62:63], v[54:55], 0, s[0:1]
	v_mov_b32_e32 v128, v60
	v_mov_b32_e32 v129, v61
	v_pk_mul_f32 v[60:61], v[98:99], v[94:95]
	v_accvgpr_read_b32 v40, a10
	v_mov_b32_e32 v102, v51
	v_mov_b32_dpp v57, v114 row_shl:1 row_mask:0xf bank_mask:0xf
	v_pk_fma_f32 v[60:61], v[114:115], v[40:41], v[60:61] op_sel_hi:[0,1,1]
	v_mov_b32_e32 v62, v115
	v_mov_b32_e32 v63, v101
	v_mov_b32_dpp v102, v113 row_shr:1 row_mask:0xf bank_mask:0xf
	v_mov_b32_e32 v105, v113
	v_pk_fma_f32 v[60:61], v[62:63], v[56:57], v[60:61]
	v_pk_mul_f32 v[62:63], v[104:105], v[102:103]
	v_mov_b32_dpp v51, v112 row_shl:1 row_mask:0xf bank_mask:0xf
	v_pk_fma_f32 v[62:63], v[112:113], v[4:5], v[62:63] op_sel_hi:[0,1,1]
	v_mov_b32_e32 v68, v113
	v_mov_b32_e32 v69, v123
	v_mov_b32_e32 v108, v49
	v_pk_fma_f32 v[62:63], v[68:69], v[50:51], v[62:63]
	v_pk_add_f32 v[60:61], v[60:61], 0 op_sel_hi:[1,0]
	v_mov_b32_dpp v108, v91 row_shr:1 row_mask:0xf bank_mask:0xf
	v_mov_b32_e32 v111, v91
	v_accvgpr_read_b32 v5, a3
	v_pk_add_f32 v[60:61], v[60:61], v[62:63]
	v_pk_mul_f32 v[62:63], v[110:111], v[108:109]
	v_accvgpr_read_b32 v4, a2
	v_mov_b32_dpp v49, v90 row_shl:1 row_mask:0xf bank_mask:0xf
	v_pk_fma_f32 v[62:63], v[90:91], v[4:5], v[62:63] op_sel_hi:[0,1,1]
	v_mov_b32_e32 v68, v91
	v_mov_b32_e32 v69, v119
	v_pk_fma_f32 v[62:63], v[68:69], v[48:49], v[62:63]
	s_mov_b64 s[0:1], 0x1430000
	v_pk_add_f32 v[60:61], v[60:61], v[62:63]
	v_lshl_add_u64 v[136:137], v[134:135], 0, s[0:1]
	s_nop 1
	s_mov_b64 vcc, s[28:29]
	s_nop 0
	v_cndmask_b32_dpp v130, v60, v128, vcc quad_perm:[1,0,3,2] row_mask:0xf bank_mask:0xf
	v_cndmask_b32_dpp v131, v61, v129, vcc quad_perm:[1,0,3,2] row_mask:0xf bank_mask:0xf
	s_mov_b64 vcc, s[30:31]
	s_nop 0
	v_cndmask_b32_dpp v132, v128, v60, vcc quad_perm:[1,0,3,2] row_mask:0xf bank_mask:0xf
	v_cndmask_b32_dpp v133, v129, v61, vcc quad_perm:[1,0,3,2] row_mask:0xf bank_mask:0xf
	global_store_dwordx4 v[136:137], v[130:133], off sc0 sc1 nt
	s_nop 1
	s_waitcnt vmcnt(12)
	s_waitcnt lgkmcnt(0)
	s_barrier
	v_accvgpr_read_b32 v2, a1
	v_accvgpr_read_b32 v12, a5
	ds_read_b64 v[60:61], v12
	ds_read_b64 v[62:63], v12 offset:288
	ds_read_b64 v[68:69], v12 offset:576
	ds_read_b64 v[70:71], v12 offset:1728
	ds_read_b64 v[72:73], v12 offset:2016
	ds_read_b64 v[82:83], v12 offset:2304
	ds_read_b64 v[80:81], v12 offset:3456
	ds_read_b64 v[84:85], v12 offset:3744
	ds_read_b64 v[116:117], v12 offset:4032
	ds_read_b64 v[114:115], v12 offset:5184
	ds_read_b64 v[112:113], v12 offset:5472
	ds_read_b64 v[90:91], v12 offset:5760
	ds_read_b32 v43, v2
	ds_read_b32 v19, v2 offset:288
	ds_read_b32 v39, v2 offset:576
	ds_read_b32 v25, v2 offset:1728
	ds_read_b32 v7, v2 offset:2016
	ds_read_b32 v21, v2 offset:2304
	ds_read_b32 v11, v2 offset:3456
	ds_read_b32 v35, v2 offset:3744
	ds_read_b32 v59, v2 offset:4032
	ds_read_b32 v57, v2 offset:5184
	ds_read_b32 v51, v2 offset:5472
	ds_read_b32 v49, v2 offset:5760
	s_waitcnt lgkmcnt(0)
	v_accvgpr_read_b32 v101, a23
	v_mov_b32_e32 v46, v43
	v_mov_b32_e32 v65, v61
	v_accvgpr_read_b32 v31, a25
	v_mov_b32_dpp v46, v61 row_shr:1 row_mask:0xf bank_mask:0xf
	v_pk_mul_f32 v[86:87], v[64:65], v[46:47]
	v_accvgpr_read_b32 v100, a22
	v_accvgpr_read_b32 v30, a24
	v_mov_b32_e32 v26, v19
	v_mov_b32_dpp v43, v60 row_shl:1 row_mask:0xf bank_mask:0xf
	v_pk_fma_f32 v[86:87], v[60:61], v[100:101], v[86:87] op_sel_hi:[0,1,1]
	v_pk_mov_b32 v[60:61], v[60:61], v[30:31] op_sel:[1,0]
	v_mov_b32_dpp v26, v63 row_shr:1 row_mask:0xf bank_mask:0xf
	v_mov_b32_e32 v1, v63
	v_pk_fma_f32 v[60:61], v[60:61], v[42:43], v[86:87]
	v_pk_mul_f32 v[86:87], v[0:1], v[26:27]
	v_accvgpr_read_b32 v0, a34
	v_accvgpr_mov_b32 a12, a14
	v_accvgpr_read_b32 v1, a35
	v_accvgpr_mov_b32 a13, a15
	v_mov_b32_dpp v19, v62 row_shl:1 row_mask:0xf bank_mask:0xf
	v_pk_fma_f32 v[86:87], v[62:63], v[16:17], v[86:87] op_sel_hi:[0,1,1]
	v_accvgpr_write_b32 a14, v16
	v_pk_mov_b32 v[62:63], v[62:63], v[0:1] op_sel:[1,0]
	v_mov_b32_e32 v44, v39
	v_accvgpr_write_b32 a15, v17
	v_pk_fma_f32 v[62:63], v[62:63], v[18:19], v[86:87]
	v_pk_add_f32 v[60:61], v[60:61], 0 op_sel_hi:[1,0]
	v_mov_b32_dpp v44, v69 row_shr:1 row_mask:0xf bank_mask:0xf
	v_accvgpr_read_b32 v16, a48
	v_mov_b32_e32 v17, v69
	v_accvgpr_read_b32 v67, a47
	v_pk_add_f32 v[60:61], v[60:61], v[62:63]
	v_pk_mul_f32 v[62:63], v[16:17], v[44:45]
	v_accvgpr_read_b32 v66, a46
	v_mov_b32_dpp v39, v68 row_shl:1 row_mask:0xf bank_mask:0xf
	v_pk_fma_f32 v[62:63], v[68:69], v[14:15], v[62:63] op_sel_hi:[0,1,1]
	v_pk_mov_b32 v[68:69], v[68:69], v[66:67] op_sel:[1,0]
	v_mov_b32_e32 v36, v25
	v_pk_fma_f32 v[62:63], v[68:69], v[38:39], v[62:63]
	s_mov_b64 s[0:1], 0x1800000
	v_pk_add_f32 v[60:61], v[60:61], v[62:63]
	v_mov_b32_dpp v36, v71 row_shr:1 row_mask:0xf bank_mask:0xf
	v_mov_b32_e32 v127, v71
	v_lshl_add_u64 v[62:63], v[54:55], 0, s[0:1]
	v_mov_b32_e32 v128, v60
	v_mov_b32_e32 v129, v61
	v_pk_mul_f32 v[60:61], v[126:127], v[36:37]
	v_mov_b32_e32 v12, v7
	v_mov_b32_dpp v25, v70 row_shl:1 row_mask:0xf bank_mask:0xf
	v_pk_fma_f32 v[60:61], v[70:71], v[8:9], v[60:61] op_sel_hi:[0,1,1]
	v_mov_b32_e32 v62, v71
	v_mov_b32_e32 v63, v31
	v_mov_b32_dpp v12, v73 row_shr:1 row_mask:0xf bank_mask:0xf
	v_mov_b32_e32 v75, v73
	v_pk_fma_f32 v[60:61], v[62:63], v[24:25], v[60:61]
	v_pk_mul_f32 v[62:63], v[74:75], v[12:13]
	v_mov_b32_dpp v7, v72 row_shl:1 row_mask:0xf bank_mask:0xf
	v_pk_fma_f32 v[62:63], v[72:73], v[22:23], v[62:63] op_sel_hi:[0,1,1]
	v_accvgpr_write_b32 a4, v22
	v_mov_b32_e32 v68, v73
	v_mov_b32_e32 v69, v1
	v_mov_b32_e32 v78, v21
	v_accvgpr_write_b32 a5, v23
	v_pk_fma_f32 v[62:63], v[68:69], v[6:7], v[62:63]
	v_pk_add_f32 v[60:61], v[60:61], 0 op_sel_hi:[1,0]
	v_mov_b32_dpp v78, v83 row_shr:1 row_mask:0xf bank_mask:0xf
	v_mov_b32_e32 v53, v83
	v_accvgpr_read_b32 v22, a26
	v_pk_add_f32 v[60:61], v[60:61], v[62:63]
	v_pk_mul_f32 v[62:63], v[52:53], v[78:79]
	v_accvgpr_read_b32 v23, a27
	v_mov_b32_dpp v21, v82 row_shl:1 row_mask:0xf bank_mask:0xf
	v_pk_fma_f32 v[62:63], v[82:83], v[22:23], v[62:63] op_sel_hi:[0,1,1]
	v_mov_b32_e32 v68, v83
	v_mov_b32_e32 v69, v67
	v_pk_fma_f32 v[62:63], v[68:69], v[20:21], v[62:63]
	v_mov_b32_e32 v76, v11
	v_pk_add_f32 v[60:61], v[60:61], v[62:63]
	s_mov_b64 s[0:1], 0x1810000
	v_mov_b32_dpp v76, v81 row_shr:1 row_mask:0xf bank_mask:0xf
	v_mov_b32_e32 v121, v81
	v_accvgpr_read_b32 v15, a13
	v_lshl_add_u64 v[136:137], v[134:135], 0, s[0:1]
	s_nop 1
	s_mov_b64 vcc, s[28:29]
	s_nop 0
	v_cndmask_b32_dpp v130, v60, v128, vcc quad_perm:[1,0,3,2] row_mask:0xf bank_mask:0xf
	v_cndmask_b32_dpp v131, v61, v129, vcc quad_perm:[1,0,3,2] row_mask:0xf bank_mask:0xf
	s_mov_b64 vcc, s[30:31]
	s_nop 0
	v_cndmask_b32_dpp v132, v128, v60, vcc quad_perm:[1,0,3,2] row_mask:0xf bank_mask:0xf
	v_cndmask_b32_dpp v133, v129, v61, vcc quad_perm:[1,0,3,2] row_mask:0xf bank_mask:0xf
	global_store_dwordx4 v[136:137], v[130:133], off sc0 sc1 nt
	s_nop 1
	v_pk_mul_f32 v[60:61], v[120:121], v[76:77]
	v_accvgpr_read_b32 v14, a12
	v_mov_b32_e32 v2, v35
	v_mov_b32_dpp v11, v80 row_shl:1 row_mask:0xf bank_mask:0xf
	v_pk_fma_f32 v[60:61], v[80:81], v[124:125], v[60:61] op_sel_hi:[0,1,1]
	v_pk_mov_b32 v[62:63], v[80:81], v[14:15] op_sel:[1,0]
	v_mov_b32_dpp v2, v85 row_shr:1 row_mask:0xf bank_mask:0xf
	v_mov_b32_e32 v107, v85
	v_pk_fma_f32 v[60:61], v[62:63], v[10:11], v[60:61]
	v_pk_mul_f32 v[62:63], v[106:107], v[2:3]
	v_mov_b32_dpp v35, v84 row_shl:1 row_mask:0xf bank_mask:0xf
	v_pk_fma_f32 v[62:63], v[84:85], v[28:29], v[62:63] op_sel_hi:[0,1,1]
	v_pk_mov_b32 v[68:69], v[84:85], v[122:123] op_sel:[1,0]
	v_mov_b32_e32 v92, v59
	v_pk_fma_f32 v[62:63], v[68:69], v[34:35], v[62:63]
	v_pk_add_f32 v[60:61], v[60:61], 0 op_sel_hi:[1,0]
	v_mov_b32_dpp v92, v117 row_shr:1 row_mask:0xf bank_mask:0xf
	v_mov_b32_e32 v97, v117
	v_accvgpr_read_b32 v87, a9
	v_pk_add_f32 v[60:61], v[60:61], v[62:63]
	v_pk_mul_f32 v[62:63], v[96:97], v[92:93]
	v_accvgpr_read_b32 v86, a8
	v_mov_b32_dpp v59, v116 row_shl:1 row_mask:0xf bank_mask:0xf
	v_pk_fma_f32 v[62:63], v[116:117], v[86:87], v[62:63] op_sel_hi:[0,1,1]
	v_pk_mov_b32 v[68:69], v[116:117], v[118:119] op_sel:[1,0]
	v_mov_b32_e32 v94, v57
	v_pk_fma_f32 v[62:63], v[68:69], v[58:59], v[62:63]
	s_mov_b64 s[0:1], 0x1820000
	v_pk_add_f32 v[60:61], v[60:61], v[62:63]
	v_mov_b32_dpp v94, v115 row_shr:1 row_mask:0xf bank_mask:0xf
	v_mov_b32_e32 v99, v115
	v_lshl_add_u64 v[62:63], v[54:55], 0, s[0:1]
	v_mov_b32_e32 v128, v60
	v_mov_b32_e32 v129, v61
	v_pk_mul_f32 v[60:61], v[98:99], v[94:95]
	v_mov_b32_e32 v102, v51
	v_mov_b32_dpp v57, v114 row_shl:1 row_mask:0xf bank_mask:0xf
	v_pk_fma_f32 v[60:61], v[114:115], v[40:41], v[60:61] op_sel_hi:[0,1,1]
	v_mov_b32_e32 v62, v115
	v_mov_b32_e32 v63, v15
	v_mov_b32_dpp v102, v113 row_shr:1 row_mask:0xf bank_mask:0xf
	v_mov_b32_e32 v105, v113
	v_accvgpr_read_b32 v89, a19
	v_pk_fma_f32 v[60:61], v[62:63], v[56:57], v[60:61]
	v_pk_mul_f32 v[62:63], v[104:105], v[102:103]
	v_accvgpr_read_b32 v88, a18
	v_mov_b32_dpp v51, v112 row_shl:1 row_mask:0xf bank_mask:0xf
	v_pk_fma_f32 v[62:63], v[112:113], v[88:89], v[62:63] op_sel_hi:[0,1,1]
	v_mov_b32_e32 v68, v113
	v_mov_b32_e32 v69, v123
	v_mov_b32_e32 v108, v49
	v_pk_fma_f32 v[62:63], v[68:69], v[50:51], v[62:63]
	v_pk_add_f32 v[60:61], v[60:61], 0 op_sel_hi:[1,0]
	v_mov_b32_dpp v108, v91 row_shr:1 row_mask:0xf bank_mask:0xf
	v_mov_b32_e32 v111, v91
	v_pk_add_f32 v[60:61], v[60:61], v[62:63]
	v_pk_mul_f32 v[62:63], v[110:111], v[108:109]
	v_mov_b32_dpp v49, v90 row_shl:1 row_mask:0xf bank_mask:0xf
	v_pk_fma_f32 v[62:63], v[90:91], v[4:5], v[62:63] op_sel_hi:[0,1,1]
	v_mov_b32_e32 v68, v91
	v_mov_b32_e32 v69, v119
	v_pk_fma_f32 v[62:63], v[68:69], v[48:49], v[62:63]
	s_mov_b64 s[0:1], 0x1830000
	v_pk_add_f32 v[60:61], v[60:61], v[62:63]
	v_lshl_add_u64 v[136:137], v[134:135], 0, s[0:1]
	s_nop 1
	s_mov_b64 vcc, s[28:29]
	s_nop 0
	v_cndmask_b32_dpp v130, v60, v128, vcc quad_perm:[1,0,3,2] row_mask:0xf bank_mask:0xf
	v_cndmask_b32_dpp v131, v61, v129, vcc quad_perm:[1,0,3,2] row_mask:0xf bank_mask:0xf
	s_mov_b64 vcc, s[30:31]
	s_nop 0
	v_cndmask_b32_dpp v132, v128, v60, vcc quad_perm:[1,0,3,2] row_mask:0xf bank_mask:0xf
	v_cndmask_b32_dpp v133, v129, v61, vcc quad_perm:[1,0,3,2] row_mask:0xf bank_mask:0xf
	global_store_dwordx4 v[136:137], v[130:133], off sc0 sc1 nt
	s_nop 1
	v_accvgpr_write_b32 a12, v28
	s_waitcnt vmcnt(8)
	v_accvgpr_write_b32 a13, v29
	v_mov_b64_e32 v[28:29], v[4:5]
	s_waitcnt lgkmcnt(0)
	s_barrier
	v_accvgpr_read_b32 v2, a6
	v_accvgpr_read_b32 v4, a7
	ds_read_b64 v[60:61], v2
	ds_read_b64 v[62:63], v2 offset:288
	ds_read_b64 v[68:69], v2 offset:576
	ds_read_b64 v[70:71], v2 offset:1728
	ds_read_b64 v[72:73], v2 offset:2016
	ds_read_b64 v[82:83], v2 offset:2304
	ds_read_b64 v[80:81], v2 offset:3456
	ds_read_b64 v[84:85], v2 offset:3744
	ds_read_b64 v[116:117], v2 offset:4032
	ds_read_b64 v[114:115], v2 offset:5184
	ds_read_b64 v[112:113], v2 offset:5472
	ds_read_b64 v[90:91], v2 offset:5760
	ds_read_b32 v43, v4
	ds_read_b32 v19, v4 offset:288
	ds_read_b32 v39, v4 offset:576
	ds_read_b32 v25, v4 offset:1728
	ds_read_b32 v7, v4 offset:2016
	ds_read_b32 v21, v4 offset:2304
	ds_read_b32 v11, v4 offset:3456
	ds_read_b32 v35, v4 offset:3744
	ds_read_b32 v59, v4 offset:4032
	ds_read_b32 v57, v4 offset:5184
	ds_read_b32 v51, v4 offset:5472
	ds_read_b32 v49, v4 offset:5760
	s_waitcnt lgkmcnt(0)
	v_accvgpr_read_b32 v8, a24
	v_mov_b32_e32 v46, v43
	v_mov_b32_e32 v65, v61
	v_mov_b32_e32 v26, v19
	v_mov_b32_dpp v46, v61 row_shr:1 row_mask:0xf bank_mask:0xf
	v_accvgpr_read_b32 v32, a32
	v_accvgpr_read_b32 v9, a25
	v_mov_b64_e32 v[124:125], v[40:41]
	v_pk_mul_f32 v[30:31], v[64:65], v[46:47]
	v_mov_b32_dpp v26, v63 row_shr:1 row_mask:0xf bank_mask:0xf
	v_mov_b32_e32 v33, v63
	v_accvgpr_read_b32 v4, a14
	v_accvgpr_read_b32 v41, a35
	v_mov_b32_e32 v44, v39
	v_pk_fma_f32 v[30:31], v[60:61], v[100:101], v[30:31] op_sel_hi:[0,1,1]
	v_mov_b32_dpp v43, v60 row_shl:1 row_mask:0xf bank_mask:0xf
	v_pk_mov_b32 v[46:47], v[60:61], v[8:9] op_sel:[1,0]
	v_pk_mul_f32 v[26:27], v[32:33], v[26:27]
	v_accvgpr_read_b32 v5, a15
	v_accvgpr_read_b32 v40, a34
	v_mov_b32_dpp v44, v69 row_shr:1 row_mask:0xf bank_mask:0xf
	v_mov_b32_e32 v17, v69
	v_accvgpr_read_b32 v0, a16
	v_pk_fma_f32 v[30:31], v[46:47], v[42:43], v[30:31]
	v_pk_fma_f32 v[26:27], v[62:63], v[4:5], v[26:27] op_sel_hi:[0,1,1]
	v_mov_b32_dpp v19, v62 row_shl:1 row_mask:0xf bank_mask:0xf
	v_pk_mov_b32 v[32:33], v[62:63], v[40:41] op_sel:[1,0]
	v_pk_mul_f32 v[16:17], v[16:17], v[44:45]
	v_accvgpr_read_b32 v1, a17
	v_pk_fma_f32 v[18:19], v[32:33], v[18:19], v[26:27]
	v_pk_add_f32 v[26:27], v[30:31], 0 op_sel_hi:[1,0]
	v_mov_b32_dpp v39, v68 row_shl:1 row_mask:0xf bank_mask:0xf
	v_pk_fma_f32 v[16:17], v[68:69], v[0:1], v[16:17] op_sel_hi:[0,1,1]
	v_pk_mov_b32 v[30:31], v[68:69], v[66:67] op_sel:[1,0]
	v_pk_add_f32 v[18:19], v[26:27], v[18:19]
	v_pk_fma_f32 v[16:17], v[30:31], v[38:39], v[16:17]
	v_mov_b32_e32 v36, v25
	s_mov_b64 s[0:1], 0x1c00000
	v_pk_add_f32 v[16:17], v[18:19], v[16:17]
	v_mov_b32_dpp v36, v71 row_shr:1 row_mask:0xf bank_mask:0xf
	v_mov_b32_e32 v127, v71
	v_accvgpr_read_b32 v0, a20
	v_lshl_add_u64 v[26:27], v[54:55], 0, s[0:1]
	v_mov_b32_e32 v128, v16
	v_mov_b32_e32 v129, v17
	v_mov_b32_e32 v12, v7
	v_pk_mul_f32 v[16:17], v[126:127], v[36:37]
	v_accvgpr_read_b32 v1, a21
	v_mov_b32_dpp v12, v73 row_shr:1 row_mask:0xf bank_mask:0xf
	v_pk_fma_f32 v[16:17], v[70:71], v[0:1], v[16:17] op_sel_hi:[0,1,1]
	v_mov_b32_e32 v75, v73
	v_accvgpr_read_b32 v0, a4
	v_mov_b32_e32 v78, v21
	v_pk_mul_f32 v[12:13], v[74:75], v[12:13]
	v_accvgpr_read_b32 v1, a5
	v_mov_b32_dpp v25, v70 row_shl:1 row_mask:0xf bank_mask:0xf
	v_mov_b32_dpp v7, v72 row_shl:1 row_mask:0xf bank_mask:0xf
	v_mov_b32_dpp v78, v83 row_shr:1 row_mask:0xf bank_mask:0xf
	v_mov_b32_e32 v8, v71
	v_pk_fma_f32 v[12:13], v[72:73], v[0:1], v[12:13] op_sel_hi:[0,1,1]
	v_mov_b32_e32 v5, v41
	v_mov_b32_e32 v4, v73
	v_mov_b32_e32 v53, v83
	v_pk_fma_f32 v[16:17], v[8:9], v[24:25], v[16:17]
	v_pk_fma_f32 v[6:7], v[4:5], v[6:7], v[12:13]
	v_pk_mul_f32 v[12:13], v[52:53], v[78:79]
	v_mov_b32_dpp v21, v82 row_shl:1 row_mask:0xf bank_mask:0xf
	v_pk_add_f32 v[16:17], v[16:17], 0 op_sel_hi:[1,0]
	v_pk_fma_f32 v[12:13], v[82:83], v[22:23], v[12:13] op_sel_hi:[0,1,1]
	v_mov_b32_e32 v66, v83
	v_pk_add_f32 v[6:7], v[16:17], v[6:7]
	v_pk_fma_f32 v[12:13], v[66:67], v[20:21], v[12:13]
	v_mov_b32_e32 v76, v11
	v_pk_add_f32 v[6:7], v[6:7], v[12:13]
	s_mov_b64 s[0:1], 0x1c10000
	v_mov_b32_dpp v76, v81 row_shr:1 row_mask:0xf bank_mask:0xf
	v_mov_b32_e32 v121, v81
	v_accvgpr_read_b32 v0, a36
	v_lshl_add_u64 v[136:137], v[134:135], 0, s[0:1]
	s_nop 1
	s_mov_b64 vcc, s[28:29]
	s_nop 0
	v_cndmask_b32_dpp v130, v6, v128, vcc quad_perm:[1,0,3,2] row_mask:0xf bank_mask:0xf
	v_cndmask_b32_dpp v131, v7, v129, vcc quad_perm:[1,0,3,2] row_mask:0xf bank_mask:0xf
	s_mov_b64 vcc, s[30:31]
	s_nop 0
	v_cndmask_b32_dpp v132, v128, v6, vcc quad_perm:[1,0,3,2] row_mask:0xf bank_mask:0xf
	v_cndmask_b32_dpp v133, v129, v7, vcc quad_perm:[1,0,3,2] row_mask:0xf bank_mask:0xf
	global_store_dwordx4 v[136:137], v[130:133], off sc0 sc1 nt
	s_nop 1
	v_mov_b32_e32 v2, v35
	v_pk_mul_f32 v[6:7], v[120:121], v[76:77]
	v_accvgpr_read_b32 v1, a37
	v_mov_b32_dpp v2, v85 row_shr:1 row_mask:0xf bank_mask:0xf
	v_pk_fma_f32 v[6:7], v[80:81], v[0:1], v[6:7] op_sel_hi:[0,1,1]
	v_mov_b32_e32 v107, v85
	v_accvgpr_read_b32 v0, a12
	v_mov_b32_e32 v92, v59
	v_pk_mul_f32 v[2:3], v[106:107], v[2:3]
	v_accvgpr_read_b32 v1, a13
	v_mov_b32_dpp v11, v80 row_shl:1 row_mask:0xf bank_mask:0xf
	v_mov_b32_dpp v35, v84 row_shl:1 row_mask:0xf bank_mask:0xf
	v_mov_b32_dpp v92, v117 row_shr:1 row_mask:0xf bank_mask:0xf
	v_pk_mov_b32 v[8:9], v[80:81], v[14:15] op_sel:[1,0]
	v_pk_fma_f32 v[2:3], v[84:85], v[0:1], v[2:3] op_sel_hi:[0,1,1]
	v_pk_mov_b32 v[4:5], v[84:85], v[122:123] op_sel:[1,0]
	v_mov_b32_e32 v97, v117
	v_pk_fma_f32 v[6:7], v[8:9], v[10:11], v[6:7]
	v_pk_fma_f32 v[0:1], v[4:5], v[34:35], v[2:3]
	v_pk_mul_f32 v[2:3], v[96:97], v[92:93]
	v_mov_b32_dpp v59, v116 row_shl:1 row_mask:0xf bank_mask:0xf
	v_pk_add_f32 v[6:7], v[6:7], 0 op_sel_hi:[1,0]
	v_pk_fma_f32 v[2:3], v[116:117], v[86:87], v[2:3] op_sel_hi:[0,1,1]
	v_pk_mov_b32 v[4:5], v[116:117], v[118:119] op_sel:[1,0]
	v_pk_add_f32 v[0:1], v[6:7], v[0:1]
	v_pk_fma_f32 v[2:3], v[4:5], v[58:59], v[2:3]
	v_mov_b32_e32 v94, v57
	v_pk_add_f32 v[0:1], v[0:1], v[2:3]
	s_mov_b64 s[0:1], 0x1c20000
	v_mov_b32_dpp v94, v115 row_shr:1 row_mask:0xf bank_mask:0xf
	v_mov_b32_e32 v102, v51
	v_mov_b32_e32 v99, v115
	v_lshl_add_u64 v[2:3], v[54:55], 0, s[0:1]
	v_mov_b32_e32 v128, v0
	v_mov_b32_e32 v129, v1
	v_mov_b32_dpp v102, v113 row_shr:1 row_mask:0xf bank_mask:0xf
	v_pk_mul_f32 v[0:1], v[98:99], v[94:95]
	v_mov_b32_e32 v105, v113
	v_mov_b32_dpp v57, v114 row_shl:1 row_mask:0xf bank_mask:0xf
	v_pk_fma_f32 v[0:1], v[114:115], v[124:125], v[0:1] op_sel_hi:[0,1,1]
	v_mov_b32_e32 v14, v115
	v_pk_mul_f32 v[2:3], v[104:105], v[102:103]
	v_mov_b32_dpp v51, v112 row_shl:1 row_mask:0xf bank_mask:0xf
	v_mov_b32_e32 v108, v49
	v_pk_fma_f32 v[0:1], v[14:15], v[56:57], v[0:1]
	v_pk_fma_f32 v[2:3], v[112:113], v[88:89], v[2:3] op_sel_hi:[0,1,1]
	v_mov_b32_e32 v122, v113
	v_mov_b32_dpp v108, v91 row_shr:1 row_mask:0xf bank_mask:0xf
	v_pk_add_f32 v[0:1], v[0:1], 0 op_sel_hi:[1,0]
	v_pk_fma_f32 v[2:3], v[122:123], v[50:51], v[2:3]
	v_mov_b32_e32 v111, v91
	v_pk_add_f32 v[0:1], v[0:1], v[2:3]
	v_pk_mul_f32 v[2:3], v[110:111], v[108:109]
	v_mov_b32_dpp v49, v90 row_shl:1 row_mask:0xf bank_mask:0xf
	v_pk_fma_f32 v[2:3], v[90:91], v[28:29], v[2:3] op_sel_hi:[0,1,1]
	v_mov_b32_e32 v118, v91
	v_pk_fma_f32 v[2:3], v[118:119], v[48:49], v[2:3]
	s_mov_b64 s[0:1], 0x1c30000
	v_pk_add_f32 v[0:1], v[0:1], v[2:3]
	v_lshl_add_u64 v[136:137], v[134:135], 0, s[0:1]
	s_nop 1
	s_mov_b64 vcc, s[28:29]
	s_nop 0
	v_cndmask_b32_dpp v130, v0, v128, vcc quad_perm:[1,0,3,2] row_mask:0xf bank_mask:0xf
	v_cndmask_b32_dpp v131, v1, v129, vcc quad_perm:[1,0,3,2] row_mask:0xf bank_mask:0xf
	s_mov_b64 vcc, s[30:31]
	s_nop 0
	v_cndmask_b32_dpp v132, v128, v0, vcc quad_perm:[1,0,3,2] row_mask:0xf bank_mask:0xf
	v_cndmask_b32_dpp v133, v129, v1, vcc quad_perm:[1,0,3,2] row_mask:0xf bank_mask:0xf
	global_store_dwordx4 v[136:137], v[130:133], off sc0 sc1 nt
	s_nop 1
	s_endpgm
